# baseline (speedup 1.0000x reference)
.LBB1_8:
	s_or_b64 exec, exec, s[4:5]
	s_waitcnt vmcnt(1)
	v_mov_b32_e32 v184, 1
	v_lshl_add_u32 v180, v176, 2, v172
	v_lshl_add_u32 v181, v177, 2, v172
	v_lshl_add_u32 v182, v178, 2, v172
	v_lshl_add_u32 v183, v179, 2, v172
	s_waitcnt lgkmcnt(0)
	ds_add_u32 v180, v184
	ds_add_u32 v181, v184
	ds_add_u32 v182, v184
	ds_add_u32 v183, v184
	s_waitcnt lgkmcnt(0)
	ds_read_b32 v151, v173
	s_waitcnt lgkmcnt(0)
	v_cvt_f32_i32_e32 v185, v151
	ds_write_b32 v173, v185 offset:256
	v_add_u32_e32 v10, v172, v2
	s_waitcnt vmcnt(1) lgkmcnt(0)
	s_barrier
	s_nop 0
	s_nop 0
	s_nop 0
	ds_read_b128 v[18:21], v10 offset:256
	ds_read_b128 v[22:25], v10 offset:288
	ds_read_b128 v[82:85], v10 offset:320
	ds_read_b128 v[86:89], v10 offset:352
	ds_read_b128 v[74:77], v10 offset:384
	ds_read_b128 v[78:81], v10 offset:416
	ds_read_b128 v[2:5], v213 offset:32768
	ds_read_b128 v[6:9], v213 offset:0
	ds_read_b128 v[66:69], v10 offset:448
	ds_read_b128 v[70:73], v10 offset:480
	ds_read_b128 v[10:13], v213 offset:1024
	s_waitcnt lgkmcnt(3)
	v_pk_mul_f32 v[26:27], v[8:9], v[20:21]
	v_pk_mul_f32 v[28:29], v[6:7], v[18:19]
	ds_read_b128 v[14:17], v213 offset:8192
	s_waitcnt lgkmcnt(1)
	v_pk_mul_f32 v[12:13], v[12:13], v[24:25]
	v_pk_mul_f32 v[10:11], v[10:11], v[22:23]
	v_pk_fma_f32 v[30:31], v[8:9], v[20:21], v[12:13]
	v_pk_fma_f32 v[32:33], v[6:7], v[18:19], v[10:11]
	v_cvt_pk_bf16_f32 v9, v12, v13
	v_cvt_pk_bf16_f32 v7, v26, v27
	v_cvt_pk_bf16_f32 v8, v10, v11
	v_cvt_pk_bf16_f32 v6, v28, v29
	ds_read_b128 v[10:13], v213 offset:33792
	s_nop 0
	v_mfma_f32_32x32x16_bf16 v[34:49], v[2:5], v[6:9], 0
	ds_read_b128 v[6:9], v213 offset:9216
	s_waitcnt lgkmcnt(2)
	v_mul_f32_e32 v26, v16, v20
	v_mul_f32_e32 v27, v17, v21
	v_pk_mul_f32 v[50:51], v[14:15], v[18:19]
	s_mov_b32 s4, 0x3727c5ac
	s_waitcnt lgkmcnt(0)
	v_pk_mul_f32 v[8:9], v[8:9], v[24:25]
	v_pk_mul_f32 v[28:29], v[6:7], v[22:23]
	v_pk_fma_f32 v[90:91], v[16:17], v[20:21], v[8:9]
	v_pk_fma_f32 v[92:93], v[14:15], v[18:19], v[28:29]
	ds_read_b128 v[14:17], v213 offset:2048
	v_cvt_pk_bf16_f32 v9, v8, v9
	v_cvt_pk_bf16_f32 v7, v26, v27
	v_cvt_pk_bf16_f32 v8, v28, v29
	ds_read_b128 v[26:29], v213 offset:3072
	v_cvt_pk_bf16_f32 v6, v50, v51
	s_waitcnt lgkmcnt(1)
	v_pk_mul_f32 v[94:95], v[14:15], v[82:83]
	s_mov_b32 s0, 0x3c800000
	v_mfma_f32_32x32x16_bf16 v[50:65], v[2:5], v[6:9], 0
	v_mul_f32_e32 v2, v16, v84
	v_mul_f32_e32 v3, v17, v85
	s_waitcnt lgkmcnt(0)
	v_mul_f32_e32 v4, v28, v88
	v_mul_f32_e32 v5, v29, v89
	v_pk_mul_f32 v[6:7], v[26:27], v[86:87]
	v_pk_fma_f32 v[8:9], v[16:17], v[84:85], v[4:5]
	v_cvt_pk_bf16_f32 v3, v2, v3
	v_pk_fma_f32 v[14:15], v[14:15], v[82:83], v[6:7]
	v_pk_add_f32 v[26:27], v[8:9], v[30:31]
	v_cvt_pk_bf16_f32 v5, v4, v5
	v_cvt_pk_bf16_f32 v4, v6, v7
	ds_read_b128 v[6:9], v213 offset:10240
	v_pk_add_f32 v[28:29], v[14:15], v[32:33]
	ds_read_b128 v[14:17], v213 offset:11264
	v_cvt_pk_bf16_f32 v2, v94, v95
	s_waitcnt lgkmcnt(1)
	v_pk_mul_f32 v[30:31], v[6:7], v[82:83]
	v_mov_b64_e32 v[152:153], s[4:5]
	v_mfma_f32_32x32x16_bf16 v[34:49], v[10:13], v[2:5], v[34:49]
	v_mul_f32_e32 v2, v8, v84
	v_mul_f32_e32 v3, v9, v85
	s_waitcnt lgkmcnt(0)
	v_mul_f32_e32 v4, v16, v88
	v_mul_f32_e32 v5, v17, v89
	v_pk_mul_f32 v[14:15], v[14:15], v[86:87]
	v_pk_fma_f32 v[8:9], v[8:9], v[84:85], v[4:5]
	v_pk_fma_f32 v[6:7], v[6:7], v[82:83], v[14:15]
	v_cvt_pk_bf16_f32 v5, v4, v5
	v_cvt_pk_bf16_f32 v3, v2, v3
	v_cvt_pk_bf16_f32 v4, v14, v15
	v_pk_add_f32 v[32:33], v[8:9], v[90:91]
	v_pk_add_f32 v[90:91], v[6:7], v[92:93]
	ds_read_b128 v[6:9], v213 offset:34816
	ds_read_b128 v[14:17], v213 offset:4096
	v_cvt_pk_bf16_f32 v2, v30, v31
	s_nop 1
	v_mfma_f32_32x32x16_bf16 v[50:65], v[10:13], v[2:5], v[50:65]
	ds_read_b128 v[2:5], v213 offset:5120
	ds_read_b128 v[10:13], v213 offset:12288
	s_waitcnt lgkmcnt(1)
	v_pk_mul_f32 v[30:31], v[16:17], v[76:77]
	v_pk_mul_f32 v[92:93], v[14:15], v[74:75]
	v_pk_mul_f32 v[4:5], v[4:5], v[80:81]
	v_pk_mul_f32 v[94:95], v[2:3], v[78:79]
	v_pk_fma_f32 v[2:3], v[16:17], v[76:77], v[4:5]
	v_cvt_pk_bf16_f32 v5, v4, v5
	v_pk_add_f32 v[96:97], v[2:3], v[26:27]
	v_cvt_pk_bf16_f32 v3, v30, v31
	v_cvt_pk_bf16_f32 v4, v94, v95
	v_cvt_pk_bf16_f32 v2, v92, v93
	v_pk_fma_f32 v[14:15], v[14:15], v[74:75], v[94:95]
	s_waitcnt lgkmcnt(0)
	v_pk_mul_f32 v[30:31], v[10:11], v[74:75]
	v_mfma_f32_32x32x16_bf16 v[34:49], v[6:9], v[2:5], v[34:49]
	ds_read_b128 v[2:5], v213 offset:13312
	v_add_f32_e32 v98, v14, v28
	v_add_f32_e32 v99, v15, v29
	ds_read_b128 v[14:17], v213 offset:35840
	v_pk_mul_f32 v[26:27], v[12:13], v[76:77]
	s_waitcnt lgkmcnt(1)
	v_pk_mul_f32 v[4:5], v[4:5], v[80:81]
	v_pk_mul_f32 v[28:29], v[2:3], v[78:79]
	v_pk_fma_f32 v[2:3], v[12:13], v[76:77], v[4:5]
	v_pk_fma_f32 v[10:11], v[10:11], v[74:75], v[28:29]
	v_pk_add_f32 v[32:33], v[2:3], v[32:33]
	v_pk_add_f32 v[92:93], v[10:11], v[90:91]
	ds_read_b128 v[10:13], v213 offset:6144
	v_cvt_pk_bf16_f32 v5, v4, v5
	v_cvt_pk_bf16_f32 v3, v26, v27
	v_cvt_pk_bf16_f32 v4, v28, v29
	ds_read_b128 v[26:29], v213 offset:7168
	v_cvt_pk_bf16_f32 v2, v30, v31
	s_waitcnt lgkmcnt(1)
	v_pk_mul_f32 v[30:31], v[10:11], v[66:67]
	v_mfma_f32_32x32x16_bf16 v[50:65], v[6:9], v[2:5], v[50:65]
	v_mul_f32_e32 v2, v12, v68
	v_mul_f32_e32 v3, v13, v69
	s_waitcnt lgkmcnt(0)
	v_mul_f32_e32 v4, v28, v72
	v_mul_f32_e32 v5, v29, v73
	v_pk_mul_f32 v[6:7], v[26:27], v[70:71]
	v_pk_fma_f32 v[8:9], v[12:13], v[68:69], v[4:5]
	v_cvt_pk_bf16_f32 v3, v2, v3
	v_pk_fma_f32 v[10:11], v[10:11], v[66:67], v[6:7]
	v_pk_add_f32 v[94:95], v[8:9], v[96:97]
	v_cvt_pk_bf16_f32 v5, v4, v5
	v_cvt_pk_bf16_f32 v4, v6, v7
	ds_read_b128 v[6:9], v213 offset:14336
	v_pk_add_f32 v[96:97], v[10:11], v[98:99]
	ds_read_b128 v[10:13], v213 offset:15360
	v_cvt_pk_bf16_f32 v2, v30, v31
	s_waitcnt lgkmcnt(1)
	v_pk_mul_f32 v[30:31], v[6:7], v[66:67]
	v_mfma_f32_32x32x16_bf16 v[34:49], v[14:17], v[2:5], v[34:49]
	s_waitcnt lgkmcnt(0)
	v_mul_f32_e32 v10, v10, v70
	v_mul_f32_e32 v11, v11, v71
	v_mul_f32_e32 v2, v8, v68
	v_mul_f32_e32 v3, v9, v69
	v_pk_mul_f32 v[4:5], v[12:13], v[72:73]
	v_pk_fma_f32 v[6:7], v[6:7], v[66:67], v[10:11]
	v_pk_fma_f32 v[8:9], v[8:9], v[68:69], v[4:5]
	v_pk_add_f32 v[92:93], v[6:7], v[92:93]
	v_cvt_pk_bf16_f32 v3, v2, v3
	v_pk_add_f32 v[90:91], v[8:9], v[32:33]
	v_cvt_pk_bf16_f32 v5, v4, v5
	v_cvt_pk_bf16_f32 v4, v10, v11
	ds_read_b128 v[26:29], v213 offset:36864
	ds_read_b128 v[6:9], v213 offset:16384
	v_cvt_pk_bf16_f32 v2, v30, v31
	ds_read_b128 v[98:101], v213 offset:25600
	ds_read_b128 v[102:105], v213 offset:37888
	v_mfma_f32_32x32x16_bf16 v[50:65], v[14:17], v[2:5], v[50:65]
	ds_read_b128 v[2:5], v213 offset:17408
	ds_read_b128 v[30:33], v213 offset:24576
	s_waitcnt lgkmcnt(1)
	v_pk_mul_f32 v[12:13], v[6:7], v[18:19]
	v_pk_mul_f32 v[10:11], v[8:9], v[20:21]
	v_pk_mul_f32 v[14:15], v[2:3], v[22:23]
	v_pk_mul_f32 v[22:23], v[98:99], v[22:23]
	v_pk_fma_f32 v[112:113], v[6:7], v[18:19], v[14:15]
	s_waitcnt lgkmcnt(0)
	v_pk_mul_f32 v[114:115], v[30:31], v[18:19]
	v_pk_fma_f32 v[118:119], v[30:31], v[18:19], v[22:23]
	v_pk_mul_f32 v[4:5], v[4:5], v[24:25]
	v_pk_mul_f32 v[106:107], v[32:33], v[20:21]
	v_pk_mul_f32 v[24:25], v[100:101], v[24:25]
	ds_read_b128 v[98:101], v213 offset:18432
	v_cvt_pk_bf16_f32 v19, v106, v107
	ds_read_b128 v[106:109], v213 offset:19456
	v_pk_fma_f32 v[110:111], v[8:9], v[20:21], v[4:5]
	v_cvt_pk_bf16_f32 v5, v4, v5
	v_cvt_pk_bf16_f32 v3, v10, v11
	v_cvt_pk_bf16_f32 v4, v14, v15
	s_waitcnt lgkmcnt(0)
	v_pk_mul_f32 v[106:107], v[106:107], v[86:87]
	v_cvt_pk_bf16_f32 v2, v12, v13
	v_pk_mul_f32 v[120:121], v[98:99], v[82:83]
	v_pk_mul_f32 v[108:109], v[108:109], v[88:89]
	v_pk_fma_f32 v[98:99], v[98:99], v[82:83], v[106:107]
	v_mfma_f32_32x32x16_bf16 v[2:17], v[26:29], v[2:5], 0
	v_cvt_pk_bf16_f32 v18, v114, v115
	v_mul_f32_e32 v114, v100, v84
	v_mul_f32_e32 v115, v101, v85
	v_fma_f32 v100, v100, v84, v108
	v_fma_f32 v101, v101, v85, v109
	v_pk_add_f32 v[124:125], v[98:99], v[112:113]
	v_pk_add_f32 v[122:123], v[100:101], v[110:111]
	v_cvt_pk_bf16_f32 v101, v108, v109
	v_cvt_pk_bf16_f32 v100, v106, v107
	ds_read_b128 v[106:109], v213 offset:26624
	v_pk_fma_f32 v[116:117], v[32:33], v[20:21], v[24:25]
	v_cvt_pk_bf16_f32 v21, v24, v25
	v_cvt_pk_bf16_f32 v20, v22, v23
	ds_read_b128 v[110:113], v213 offset:27648
	v_cvt_pk_bf16_f32 v99, v114, v115
	v_mfma_f32_32x32x16_bf16 v[18:33], v[26:29], v[18:21], 0
	v_cvt_pk_bf16_f32 v98, v120, v121
	s_waitcnt lgkmcnt(0)
	v_mul_f32_e32 v114, v106, v82
	v_mul_f32_e32 v115, v107, v83
	v_pk_mul_f32 v[86:87], v[110:111], v[86:87]
	v_pk_mul_f32 v[88:89], v[112:113], v[88:89]
	v_pk_fma_f32 v[82:83], v[106:107], v[82:83], v[86:87]
	v_mfma_f32_32x32x16_bf16 v[2:17], v[102:105], v[98:101], v[2:17]
	v_mul_f32_e32 v98, v108, v84
	v_mul_f32_e32 v99, v109, v85
	v_fma_f32 v84, v108, v84, v88
	v_fma_f32 v85, v109, v85, v89
	v_add_f32_e32 v108, v82, v118
	v_add_f32_e32 v109, v83, v119
	v_cvt_pk_bf16_f32 v83, v98, v99
	v_pk_add_f32 v[106:107], v[84:85], v[116:117]
	v_cvt_pk_bf16_f32 v85, v88, v89
	v_cvt_pk_bf16_f32 v84, v86, v87
	ds_read_b128 v[86:89], v213 offset:38912
	ds_read_b128 v[98:101], v213 offset:20480
	v_cvt_pk_bf16_f32 v82, v114, v115
	s_waitcnt lgkmcnt(0)
	v_pk_mul_f32 v[110:111], v[100:101], v[76:77]
	v_mfma_f32_32x32x16_bf16 v[18:33], v[102:105], v[82:85], v[18:33]
	ds_read_b128 v[82:85], v213 offset:21504
	ds_read_b128 v[102:105], v213 offset:28672
	v_mul_f32_e32 v112, v98, v74
	v_mul_f32_e32 v113, v99, v75
	s_waitcnt lgkmcnt(1)
	v_pk_mul_f32 v[84:85], v[84:85], v[80:81]
	v_pk_mul_f32 v[114:115], v[82:83], v[78:79]
	v_pk_fma_f32 v[82:83], v[100:101], v[76:77], v[84:85]
	v_cvt_pk_bf16_f32 v85, v84, v85
	v_pk_add_f32 v[116:117], v[82:83], v[122:123]
	v_cvt_pk_bf16_f32 v83, v110, v111
	v_cvt_pk_bf16_f32 v84, v114, v115
	v_cvt_pk_bf16_f32 v82, v112, v113
	v_pk_fma_f32 v[98:99], v[98:99], v[74:75], v[114:115]
	s_waitcnt lgkmcnt(0)
	v_pk_mul_f32 v[112:113], v[102:103], v[74:75]
	v_mfma_f32_32x32x16_bf16 v[2:17], v[86:89], v[82:85], v[2:17]
	ds_read_b128 v[82:85], v213 offset:29696
	v_add_f32_e32 v118, v98, v124
	v_add_f32_e32 v119, v99, v125
	v_mul_f32_e32 v110, v104, v76
	v_mul_f32_e32 v111, v105, v77
	ds_read_b128 v[98:101], v213 offset:39936
	s_waitcnt lgkmcnt(1)
	v_pk_mul_f32 v[78:79], v[82:83], v[78:79]
	v_pk_mul_f32 v[80:81], v[84:85], v[80:81]
	v_pk_fma_f32 v[74:75], v[102:103], v[74:75], v[78:79]
	v_pk_fma_f32 v[76:77], v[104:105], v[76:77], v[80:81]
	v_pk_add_f32 v[104:105], v[74:75], v[108:109]
	v_pk_add_f32 v[102:103], v[76:77], v[106:107]
	v_cvt_pk_bf16_f32 v77, v80, v81
	v_cvt_pk_bf16_f32 v76, v78, v79
	ds_read_b128 v[78:81], v213 offset:22528
	ds_read_b128 v[82:85], v213 offset:23552
	v_cvt_pk_bf16_f32 v75, v110, v111
	v_cvt_pk_bf16_f32 v74, v112, v113
	s_waitcnt lgkmcnt(0)
	v_pk_mul_f32 v[82:83], v[82:83], v[70:71]
	v_mfma_f32_32x32x16_bf16 v[18:33], v[86:89], v[74:77], v[18:33]
	v_mul_f32_e32 v74, v80, v68
	v_mul_f32_e32 v75, v81, v69
	v_mul_f32_e32 v76, v84, v72
	v_mul_f32_e32 v77, v85, v73
	v_mul_f32_e32 v86, v78, v66
	v_mul_f32_e32 v87, v79, v67
	v_pk_fma_f32 v[80:81], v[80:81], v[68:69], v[76:77]
	v_pk_fma_f32 v[78:79], v[78:79], v[66:67], v[82:83]
	v_cvt_pk_bf16_f32 v75, v74, v75
	v_pk_add_f32 v[88:89], v[80:81], v[116:117]
	v_pk_add_f32 v[106:107], v[78:79], v[118:119]
	ds_read_b128 v[78:81], v213 offset:30720
	v_cvt_pk_bf16_f32 v77, v76, v77
	v_cvt_pk_bf16_f32 v76, v82, v83
	ds_read_b128 v[82:85], v213 offset:31744
	v_cvt_pk_bf16_f32 v74, v86, v87
	s_waitcnt lgkmcnt(0)
	v_pk_mul_f32 v[72:73], v[84:85], v[72:73]
	v_mfma_f32_32x32x16_bf16 v[2:17], v[98:101], v[74:77], v[2:17]
	v_mul_f32_e32 v74, v80, v68
	v_mul_f32_e32 v75, v81, v69
	v_fma_f32 v68, v80, v68, v72
	v_fma_f32 v69, v81, v69, v73
	v_mul_f32_e32 v70, v82, v70
	v_mul_f32_e32 v71, v83, v71
	v_pk_add_f32 v[84:85], v[68:69], v[102:103]
	v_cvt_pk_bf16_f32 v69, v72, v73
	v_add_f32_e32 v72, v97, v96
	v_add_f32_e32 v73, v94, v95
	v_pk_mul_f32 v[76:77], v[78:79], v[66:67]
	v_pk_fma_f32 v[66:67], v[78:79], v[66:67], v[70:71]
	v_add_f32_e32 v72, v72, v73
	v_pk_add_f32 v[86:87], v[66:67], v[104:105]
	v_mov_b32_e32 v66, v72
	s_nop 1
	v_permlane32_swap_b32_e32 v72, v66
	v_add_f32_e32 v66, v72, v66
	v_cvt_pk_bf16_f32 v67, v74, v75
	v_rcp_f32_e32 v74, v66
	v_cvt_pk_bf16_f32 v68, v70, v71
	v_cvt_pk_bf16_f32 v66, v76, v77
	v_pk_mul_f32 v[70:71], v[46:47], v[74:75] op_sel_hi:[1,0]
	s_nop 0
	v_mfma_f32_32x32x16_bf16 v[18:33], v[98:101], v[66:69], v[18:33]
	v_mul_f32_e32 v66, v42, v74
	v_mul_f32_e32 v67, v43, v74
	v_add_f32_e32 v42, v93, v92
	v_add_f32_e32 v43, v90, v91
	v_pk_mul_f32 v[68:69], v[44:45], v[74:75] op_sel_hi:[1,0]
	v_add_f32_e32 v42, v42, v43
	v_mov_b32_e32 v43, v42
	s_nop 1
	v_permlane32_swap_b32_e32 v42, v43
	v_add_f32_e32 v42, v42, v43
	v_rcp_f32_e32 v42, v42
	v_add_f32_e32 v44, v107, v106
	v_add_f32_e32 v45, v88, v89
	v_pk_mul_f32 v[72:73], v[48:49], v[74:75] op_sel_hi:[1,0]
	v_add_f32_e32 v44, v44, v45
	v_pk_mul_f32 v[36:37], v[36:37], v[74:75] op_sel_hi:[1,0]
	v_pk_mul_f32 v[38:39], v[38:39], v[74:75] op_sel_hi:[1,0]
	v_pk_mul_f32 v[40:41], v[40:41], v[74:75] op_sel_hi:[1,0]
	v_pk_mul_f32 v[34:35], v[34:35], v[74:75] op_sel_hi:[1,0]
	v_pk_mul_f32 v[74:75], v[58:59], v[42:43] op_sel_hi:[1,0]
	v_pk_mul_f32 v[78:79], v[60:61], v[42:43] op_sel_hi:[1,0]
	v_pk_mul_f32 v[80:81], v[62:63], v[42:43] op_sel_hi:[1,0]
	v_pk_mul_f32 v[82:83], v[64:65], v[42:43] op_sel_hi:[1,0]
	v_pk_mul_f32 v[92:93], v[52:53], v[42:43] op_sel_hi:[1,0]
	v_mov_b32_e32 v43, v44
	s_nop 1
	v_permlane32_swap_b32_e32 v44, v43
	v_add_f32_e32 v43, v44, v43
	v_rcp_f32_e32 v76, v43
	v_pk_mul_f32 v[96:97], v[54:55], v[42:43] op_sel_hi:[1,0]
	v_pk_mul_f32 v[94:95], v[56:57], v[42:43] op_sel_hi:[1,0]
	v_pk_mul_f32 v[98:99], v[50:51], v[42:43] op_sel_hi:[1,0]
	v_pk_mul_f32 v[100:101], v[4:5], v[76:77] op_sel_hi:[1,0]
	v_pk_mov_b32 v[4:5], v[86:87], v[84:85] op_sel:[1,0]
	v_mov_b32_e32 v87, v85
	v_pk_add_f32 v[4:5], v[4:5], v[86:87]
	v_pk_mul_f32 v[102:103], v[6:7], v[76:77] op_sel_hi:[1,0]
	v_pk_add_f32 v[104:105], v[4:5], v[4:5] op_sel:[0,1] op_sel_hi:[1,0]
	v_cvt_pk_bf16_f32 v7, v40, v41
	ds_read_b128 v[84:87], v150 offset:52224
	ds_read_b128 v[50:53], v150 offset:35840
	ds_read_b128 v[54:57], v150 offset:36864
	ds_read_b128 v[58:61], v150 offset:37888
	ds_read_b128 v[62:65], v150 offset:38912
	v_cvt_pk_bf16_f32 v6, v38, v39
	v_cvt_pk_bf16_f32 v5, v36, v37
	v_cvt_pk_bf16_f32 v4, v34, v35
	ds_read_b128 v[88:91], v150 offset:53248
	ds_read_b128 v[34:37], v150 offset:39936
	ds_read_b128 v[38:41], v150 offset:40960
	ds_read_b128 v[42:45], v150 offset:41984
	ds_read_b128 v[46:49], v150 offset:43008
	v_cvt_pk_bf16_f32 v95, v94, v95
	v_cvt_pk_bf16_f32 v94, v96, v97
	v_cvt_pk_bf16_f32 v93, v92, v93
	v_cvt_pk_bf16_f32 v92, v98, v99
	s_waitcnt lgkmcnt(5)
	v_mfma_f32_32x32x16_bf16 v[50:65], v[84:87], v[4:7], v[50:65]
	v_mul_f32_e32 v10, v10, v76
	v_mul_f32_e32 v11, v11, v76
	v_mul_f32_e32 v12, v12, v76
	v_mul_f32_e32 v13, v13, v76
	v_mul_f32_e32 v8, v8, v76
	v_mul_f32_e32 v9, v9, v76
	v_mov_b32_e32 v77, v104
	s_nop 1
	v_permlane32_swap_b32_e32 v104, v77
	v_cvt_pk_bf16_f32 v73, v72, v73
	s_waitcnt lgkmcnt(0)
	v_mfma_f32_32x32x16_bf16 v[34:49], v[84:87], v[92:95], v[34:49]
	v_cvt_pk_bf16_f32 v72, v70, v71
	v_cvt_pk_bf16_f32 v70, v66, v67
	v_add_f32_e32 v66, v104, v77
	v_cvt_pk_bf16_f32 v71, v68, v69
	v_rcp_f32_e32 v104, v66
	v_cvt_pk_bf16_f32 v69, v82, v83
	v_cvt_pk_bf16_f32 v68, v80, v81
	v_cvt_pk_bf16_f32 v67, v78, v79
	v_cvt_pk_bf16_f32 v66, v74, v75
	ds_read_b128 v[78:81], v150 offset:54272
	v_mfma_f32_32x32x16_bf16 v[50:65], v[88:91], v[70:73], v[50:65]
	v_mul_f32_e32 v2, v2, v76
	v_mul_f32_e32 v3, v3, v76
	v_mul_f32_e32 v20, v20, v104
	v_mul_f32_e32 v21, v21, v104
	v_cvt_pk_bf16_f32 v85, v8, v9
	v_cvt_pk_bf16_f32 v82, v2, v3
	v_pk_mul_f32 v[2:3], v[22:23], v[104:105] op_sel_hi:[1,0]
	v_pk_mul_f32 v[8:9], v[24:25], v[104:105] op_sel_hi:[1,0]
	v_pk_mul_f32 v[18:19], v[18:19], v[104:105] op_sel_hi:[1,0]
	v_mfma_f32_32x32x16_bf16 v[34:49], v[88:91], v[66:69], v[34:49]
	v_cvt_pk_bf16_f32 v84, v102, v103
	v_cvt_pk_bf16_f32 v83, v100, v101
	ds_read_b128 v[86:89], v150 offset:55296
	v_cvt_pk_bf16_f32 v99, v8, v9
	v_cvt_pk_bf16_f32 v98, v2, v3
	v_cvt_pk_bf16_f32 v97, v20, v21
	v_cvt_pk_bf16_f32 v96, v18, v19
	s_waitcnt lgkmcnt(1)
	v_mfma_f32_32x32x16_bf16 v[50:65], v[78:81], v[82:85], v[50:65]
	v_mul_f32_e32 v2, v14, v76
	v_mul_f32_e32 v3, v15, v76
	v_mul_f32_e32 v8, v16, v76
	v_mul_f32_e32 v9, v17, v76
	v_mul_f32_e32 v14, v26, v104
	v_mul_f32_e32 v15, v27, v104
	v_cvt_pk_bf16_f32 v77, v8, v9
	v_cvt_pk_bf16_f32 v76, v2, v3
	v_cvt_pk_bf16_f32 v74, v10, v11
	v_pk_mul_f32 v[2:3], v[28:29], v[104:105] op_sel_hi:[1,0]
	v_mfma_f32_32x32x16_bf16 v[34:49], v[78:81], v[96:99], v[34:49]
	v_mul_f32_e32 v8, v30, v104
	v_mul_f32_e32 v9, v31, v104
	v_mul_f32_e32 v10, v32, v104
	v_mul_f32_e32 v11, v33, v104
	v_cvt_pk_bf16_f32 v75, v12, v13
	v_cvt_pk_bf16_f32 v81, v10, v11
	v_cvt_pk_bf16_f32 v80, v8, v9
	v_cvt_pk_bf16_f32 v79, v2, v3
	v_cvt_pk_bf16_f32 v78, v14, v15
	s_waitcnt lgkmcnt(0)
	v_mfma_f32_32x32x16_bf16 v[50:65], v[86:89], v[74:77], v[50:65]
	v_mfma_f32_32x32x16_bf16 v[34:49], v[86:89], v[78:81], v[34:49]
	ds_read_b128 v[86:89], v150 offset:56320
	ds_read_b128 v[18:21], v150 offset:44032
	ds_read_b128 v[22:25], v150 offset:45056
	ds_read_b128 v[26:29], v150 offset:46080
	ds_read_b128 v[30:33], v150 offset:47104
	ds_read_b128 v[100:103], v150 offset:57344
	s_waitcnt lgkmcnt(1)
	v_mfma_f32_32x32x16_bf16 v[18:33], v[86:89], v[4:7], v[18:33]
	ds_read_b128 v[2:5], v150 offset:48128
	ds_read_b128 v[6:9], v150 offset:49152
	ds_read_b128 v[10:13], v150 offset:50176
	ds_read_b128 v[14:17], v150 offset:51200
	s_waitcnt lgkmcnt(0)
	v_mfma_f32_32x32x16_bf16 v[2:17], v[86:89], v[92:95], v[2:17]
	v_mfma_f32_32x32x16_bf16 v[18:33], v[100:103], v[70:73], v[18:33]
	v_mfma_f32_32x32x16_bf16 v[2:17], v[100:103], v[66:69], v[2:17]
	ds_read_b128 v[66:69], v150 offset:58368
	ds_read_b128 v[70:73], v150 offset:59392
	s_waitcnt lgkmcnt(1)
	v_mfma_f32_32x32x16_bf16 v[18:33], v[66:69], v[82:85], v[18:33]
	v_mfma_f32_32x32x16_bf16 v[2:17], v[66:69], v[96:99], v[2:17]
	s_waitcnt lgkmcnt(0)
	v_mfma_f32_32x32x16_bf16 v[18:33], v[70:73], v[74:77], v[18:33]
	v_mfma_f32_32x32x16_bf16 v[2:17], v[70:73], v[78:81], v[2:17]
	s_nop 10
	v_mul_f32_e32 v66, v22, v22
	v_mul_f32_e32 v67, v23, v23
	v_mul_f32_e32 v68, v30, v30
	v_mul_f32_e32 v69, v31, v31
	v_mul_f32_e32 v70, v24, v24
	v_mul_f32_e32 v71, v25, v25
	v_pk_mul_f32 v[72:73], v[32:33], v[32:33]
	v_pk_mul_f32 v[74:75], v[20:21], v[20:21]
	v_pk_mul_f32 v[76:77], v[28:29], v[28:29]
	v_pk_mul_f32 v[78:79], v[26:27], v[26:27]
	v_pk_mul_f32 v[80:81], v[18:19], v[18:19]
	v_pk_fma_f32 v[78:79], v[58:59], v[58:59], v[78:79]
	v_pk_fma_f32 v[76:77], v[60:61], v[60:61], v[76:77]
	v_pk_fma_f32 v[74:75], v[52:53], v[52:53], v[74:75]
	v_pk_fma_f32 v[72:73], v[64:65], v[64:65], v[72:73]
	v_pk_fma_f32 v[70:71], v[56:57], v[56:57], v[70:71]
	v_pk_fma_f32 v[68:69], v[62:63], v[62:63], v[68:69]
	v_pk_fma_f32 v[66:67], v[54:55], v[54:55], v[66:67]
	v_pk_fma_f32 v[80:81], v[50:51], v[50:51], v[80:81]
	v_pk_add_f32 v[66:67], v[66:67], v[68:69]
	v_pk_add_f32 v[68:69], v[70:71], v[72:73]
	v_pk_add_f32 v[70:71], v[74:75], v[76:77]
	v_pk_add_f32 v[72:73], v[80:81], v[78:79]
	v_pk_add_f32 v[68:69], v[70:71], v[68:69]
	v_pk_add_f32 v[66:67], v[72:73], v[66:67]
	v_pk_mul_f32 v[72:73], v[14:15], v[14:15]
	v_pk_mov_b32 v[70:71], v[66:67], v[68:69] op_sel:[1,0]
	v_mov_b32_e32 v67, v69
	v_pk_add_f32 v[66:67], v[70:71], v[66:67]
	v_pk_mul_f32 v[70:71], v[6:7], v[6:7]
	v_pk_mul_f32 v[74:75], v[8:9], v[8:9]
	v_pk_mul_f32 v[76:77], v[16:17], v[16:17]
	v_pk_mul_f32 v[78:79], v[4:5], v[4:5]
	v_pk_mul_f32 v[80:81], v[12:13], v[12:13]
	v_pk_mul_f32 v[82:83], v[10:11], v[10:11]
	v_pk_mul_f32 v[84:85], v[2:3], v[2:3]
	v_pk_fma_f32 v[82:83], v[42:43], v[42:43], v[82:83]
	v_pk_fma_f32 v[80:81], v[44:45], v[44:45], v[80:81]
	v_pk_fma_f32 v[78:79], v[36:37], v[36:37], v[78:79]
	v_pk_fma_f32 v[76:77], v[48:49], v[48:49], v[76:77]
	v_pk_fma_f32 v[74:75], v[40:41], v[40:41], v[74:75]
	v_pk_fma_f32 v[72:73], v[46:47], v[46:47], v[72:73]
	v_pk_fma_f32 v[70:71], v[38:39], v[38:39], v[70:71]
	v_pk_fma_f32 v[84:85], v[34:35], v[34:35], v[84:85]
	v_pk_add_f32 v[70:71], v[70:71], v[72:73]
	v_pk_add_f32 v[72:73], v[74:75], v[76:77]
	v_pk_add_f32 v[74:75], v[78:79], v[80:81]
	v_pk_add_f32 v[76:77], v[84:85], v[82:83]
	v_pk_add_f32 v[72:73], v[74:75], v[72:73]
	v_pk_add_f32 v[70:71], v[76:77], v[70:71]
	v_pk_add_f32 v[66:67], v[66:67], v[66:67] op_sel:[0,1] op_sel_hi:[1,0]
	v_add_f32_e32 v70, v71, v70
	v_add_f32_e32 v71, v72, v73
	v_mov_b32_e32 v69, v66
	v_add_f32_e32 v70, v70, v71
	s_nop 0
	v_permlane32_swap_b32_e32 v66, v69
	v_mov_b32_e32 v68, v70
	s_nop 1
	v_permlane32_swap_b32_e32 v70, v68
	v_mov_b32_e32 v71, v66
	v_pk_add_f32 v[66:67], v[70:71], v[68:69]
	v_pk_fma_f32 v[66:67], v[66:67], s[0:1], v[152:153] op_sel_hi:[1,0,0]
	s_mov_b32 s1, 0x800000
	v_rsq_f32_e32 v68, v67
	s_nop 0
	v_pk_mul_f32 v[158:159], v[50:51], v[68:69] op_sel_hi:[1,0]
	v_pk_mul_f32 v[50:51], v[18:19], v[68:69] op_sel_hi:[1,0]
	v_pk_mul_f32 v[80:81], v[60:61], v[68:69] op_sel_hi:[1,0]
	v_pk_mul_f32 v[60:61], v[28:29], v[68:69] op_sel_hi:[1,0]
	v_pk_mul_f32 v[78:79], v[58:59], v[68:69] op_sel_hi:[1,0]
	v_pk_mul_f32 v[160:161], v[52:53], v[68:69] op_sel_hi:[1,0]
	v_pk_mul_f32 v[82:83], v[54:55], v[68:69] op_sel_hi:[1,0]
	v_rsq_f32_e32 v28, v66
	v_pk_mul_f32 v[168:169], v[56:57], v[68:69] op_sel_hi:[1,0]
	v_pk_mul_f32 v[58:59], v[26:27], v[68:69] op_sel_hi:[1,0]
	v_pk_mul_f32 v[52:53], v[20:21], v[68:69] op_sel_hi:[1,0]
	v_pk_mul_f32 v[54:55], v[22:23], v[68:69] op_sel_hi:[1,0]
	v_pk_mul_f32 v[56:57], v[24:25], v[68:69] op_sel_hi:[1,0]
	v_pk_mul_f32 v[18:19], v[42:43], v[28:29] op_sel_hi:[1,0]
	v_pk_mul_f32 v[20:21], v[44:45], v[28:29] op_sel_hi:[1,0]
	v_pk_mul_f32 v[22:23], v[46:47], v[28:29] op_sel_hi:[1,0]
	v_pk_mul_f32 v[26:27], v[48:49], v[28:29] op_sel_hi:[1,0]
	v_pk_mul_f32 v[162:163], v[34:35], v[28:29] op_sel_hi:[1,0]
	v_pk_mul_f32 v[164:165], v[36:37], v[28:29] op_sel_hi:[1,0]
	v_pk_mul_f32 v[166:167], v[38:39], v[28:29] op_sel_hi:[1,0]
	v_pk_mul_f32 v[24:25], v[40:41], v[28:29] op_sel_hi:[1,0]
	v_pk_mul_f32 v[104:105], v[2:3], v[28:29] op_sel_hi:[1,0]
	v_pk_mul_f32 v[112:113], v[4:5], v[28:29] op_sel_hi:[1,0]
	ds_read_b128 v[2:5], v150 offset:60416
	ds_read_b128 v[34:37], v174 offset:32768
	ds_read_b128 v[38:41], v174 offset:32800
	ds_read_b128 v[42:45], v174 offset:32832
	ds_read_b128 v[46:49], v174 offset:32864
	v_cvt_pk_bf16_f32 v129, v168, v169
	v_cvt_pk_bf16_f32 v128, v82, v83
	v_cvt_pk_bf16_f32 v127, v160, v161
	v_cvt_pk_bf16_f32 v126, v158, v159
	v_cvt_pk_bf16_f32 v137, v24, v25
	v_cvt_pk_bf16_f32 v136, v166, v167
	v_cvt_pk_bf16_f32 v135, v164, v165
	s_waitcnt lgkmcnt(0)
	v_mfma_f32_32x32x16_bf16 v[86:101], v[2:5], v[126:129], v[34:49]
	v_cvt_pk_bf16_f32 v134, v162, v163
	v_mul_f32_e32 v84, v62, v68
	v_mul_f32_e32 v85, v63, v68
	v_mul_f32_e32 v170, v64, v68
	v_mul_f32_e32 v171, v65, v68
	v_pk_mul_f32 v[62:63], v[30:31], v[68:69] op_sel_hi:[1,0]
	v_pk_mul_f32 v[64:65], v[32:33], v[68:69] op_sel_hi:[1,0]
	v_pk_mul_f32 v[116:117], v[6:7], v[28:29] op_sel_hi:[1,0]
	v_pk_mul_f32 v[154:155], v[8:9], v[28:29] op_sel_hi:[1,0]
	v_mfma_f32_32x32x16_bf16 v[34:49], v[2:5], v[134:137], v[34:49]
	ds_read_b128 v[6:9], v150 offset:61440
	ds_read_b128 v[66:69], v174 offset:32896
	ds_read_b128 v[106:109], v150 offset:64512
	v_cvt_pk_bf16_f32 v125, v170, v171
	v_cvt_pk_bf16_f32 v124, v84, v85
	v_cvt_pk_bf16_f32 v123, v80, v81
	v_cvt_pk_bf16_f32 v122, v78, v79
	v_cvt_pk_bf16_f32 v149, v26, v27
	v_cvt_pk_bf16_f32 v148, v22, v23
	v_cvt_pk_bf16_f32 v147, v20, v21
	v_cvt_pk_bf16_f32 v146, v18, v19
	s_waitcnt lgkmcnt(2)
	v_mfma_f32_32x32x16_bf16 v[86:101], v[6:9], v[122:125], v[86:101]
	v_mul_f32_e32 v102, v10, v28
	v_mul_f32_e32 v103, v11, v28
	v_mul_f32_e32 v110, v12, v28
	v_mul_f32_e32 v111, v13, v28
	v_mul_f32_e32 v114, v14, v28
	v_mul_f32_e32 v115, v15, v28
	v_pk_mul_f32 v[156:157], v[16:17], v[28:29] op_sel_hi:[1,0]
	ds_read_b128 v[176:179], v174 offset:33536
	ds_read_b128 v[180:183], v174 offset:33568
	ds_read_b128 v[184:187], v174 offset:33600
	ds_read_b128 v[28:31], v174 offset:33632
	ds_read_b128 v[188:191], v174 offset:33792
	ds_read_b128 v[192:195], v174 offset:33824
	ds_read_b128 v[196:199], v174 offset:33856
	ds_read_b128 v[200:203], v174 offset:33888
	ds_read_b128 v[204:207], v150 offset:62464
	v_cvt_pk_bf16_f32 v133, v56, v57
	v_mfma_f32_32x32x16_bf16 v[34:49], v[6:9], v[146:149], v[34:49]
	v_cvt_pk_bf16_f32 v132, v54, v55
	v_cvt_pk_bf16_f32 v131, v52, v53
	v_cvt_pk_bf16_f32 v130, v50, v51
	ds_read_b128 v[70:73], v174 offset:33664
	ds_read_b128 v[74:77], v174 offset:33920
	ds_read_b128 v[208:211], v150 offset:63488
	v_cvt_pk_bf16_f32 v145, v154, v155
	v_cvt_pk_bf16_f32 v144, v116, v117
	v_cvt_pk_bf16_f32 v143, v112, v113
	v_cvt_pk_bf16_f32 v142, v104, v105
	s_waitcnt lgkmcnt(3)
	v_mfma_f32_32x32x16_bf16 v[86:101], v[204:207], v[130:133], v[86:101]
	v_cvt_pk_bf16_f32 v121, v64, v65
	v_cvt_pk_bf16_f32 v120, v62, v63
	v_cvt_pk_bf16_f32 v119, v60, v61
	v_cvt_pk_bf16_f32 v118, v58, v59
	v_cvt_pk_bf16_f32 v141, v156, v157
	v_cvt_pk_bf16_f32 v140, v114, v115
	v_cvt_pk_bf16_f32 v139, v110, v111
	v_mfma_f32_32x32x16_bf16 v[34:49], v[204:207], v[142:145], v[34:49]
	v_cvt_pk_bf16_f32 v138, v102, v103
	v_fma_f32 v16, v30, v170, v202
	v_fma_f32 v17, v31, v171, v203
	v_fma_f32 v14, v28, v84, v200
	v_fma_f32 v15, v29, v85, v201
	v_pk_fma_f32 v[12:13], v[186:187], v[80:81], v[198:199]
	v_pk_fma_f32 v[10:11], v[184:185], v[78:79], v[196:197]
	v_pk_fma_f32 v[8:9], v[182:183], v[168:169], v[194:195]
	s_waitcnt lgkmcnt(0)
	v_mfma_f32_32x32x16_bf16 v[86:101], v[208:211], v[118:121], v[86:101]
	v_fma_f32 v6, v180, v82, v192
	v_fma_f32 v7, v181, v83, v193
	ds_read_b128 v[78:81], v174 offset:33760
	ds_read_b128 v[82:85], v174 offset:33248
	v_fma_f32 v4, v178, v160, v190
	v_fma_f32 v5, v179, v161, v191
	v_pk_fma_f32 v[2:3], v[176:177], v[158:159], v[188:189]
	v_pk_fma_f32 v[32:33], v[30:31], v[26:27], v[202:203]
	v_pk_fma_f32 v[30:31], v[28:29], v[22:23], v[200:201]
	v_pk_fma_f32 v[28:29], v[186:187], v[20:21], v[198:199]
	v_pk_fma_f32 v[26:27], v[184:185], v[18:19], v[196:197]
	v_pk_fma_f32 v[24:25], v[182:183], v[24:25], v[194:195]
	v_pk_fma_f32 v[22:23], v[180:181], v[166:167], v[192:193]
	v_pk_fma_f32 v[20:21], v[178:179], v[164:165], v[190:191]
	v_pk_fma_f32 v[18:19], v[176:177], v[162:163], v[188:189]
	ds_read_b128 v[158:161], v174 offset:33696
	ds_read_b128 v[162:165], v174 offset:33728
	ds_read_b128 v[166:169], v174 offset:33952
	ds_read_b128 v[176:179], v174 offset:33984
	ds_read_b128 v[180:183], v174 offset:34016
	ds_read_b128 v[184:187], v212 offset:11264
	v_mfma_f32_32x32x16_bf16 v[34:49], v[208:211], v[138:141], v[34:49]
	v_cvt_pk_bf16_f32 v86, v86, v87
	v_cvt_pk_bf16_f32 v87, v88, v89
	v_cvt_pk_bf16_f32 v88, v90, v91
	v_cvt_pk_bf16_f32 v89, v92, v93
	ds_read_b128 v[90:93], v212 offset:12288
	v_pk_max_i16 v86, v86, 0
	v_pk_max_i16 v87, v87, 0
	v_pk_max_i16 v88, v88, 0
	v_pk_max_i16 v89, v89, 0
	s_nop 1
	s_nop 0
	v_cvt_pk_bf16_f32 v188, v34, v35
	v_cvt_pk_bf16_f32 v189, v36, v37
	v_cvt_pk_bf16_f32 v190, v38, v39
	v_cvt_pk_bf16_f32 v191, v40, v41
	s_waitcnt lgkmcnt(1)
	v_mfma_f32_32x32x16_bf16 v[2:17], v[184:187], v[86:89], v[2:17]
	v_pk_max_i16 v188, v188, 0
	v_pk_max_i16 v189, v189, 0
	v_pk_max_i16 v190, v190, 0
	v_pk_max_i16 v191, v191, 0
	v_cvt_pk_bf16_f32 v94, v94, v95
	v_cvt_pk_bf16_f32 v95, v96, v97
	v_cvt_pk_bf16_f32 v96, v98, v99
	v_cvt_pk_bf16_f32 v97, v100, v101
	v_cvt_pk_bf16_f32 v98, v42, v43
	v_cvt_pk_bf16_f32 v99, v44, v45
	v_mfma_f32_32x32x16_bf16 v[18:33], v[184:187], v[188:191], v[18:33]
	ds_read_b128 v[184:187], v212 offset:19456
	v_cvt_pk_bf16_f32 v100, v46, v47
	v_cvt_pk_bf16_f32 v101, v48, v49
	v_fma_f32 v64, v80, v64, v182
	v_fma_f32 v65, v81, v65, v183
	v_pk_fma_f32 v[62:63], v[78:79], v[62:63], v[180:181]
	v_pk_fma_f32 v[60:61], v[164:165], v[60:61], v[178:179]
	v_pk_fma_f32 v[58:59], v[162:163], v[58:59], v[176:177]
	v_pk_max_i16 v94, v94, 0
	v_pk_max_i16 v95, v95, 0
	v_pk_max_i16 v96, v96, 0
	v_pk_max_i16 v97, v97, 0
	v_pk_max_i16 v98, v98, 0
	v_pk_max_i16 v99, v99, 0
	v_pk_max_i16 v100, v100, 0
	v_pk_max_i16 v101, v101, 0
	v_pk_fma_f32 v[56:57], v[160:161], v[56:57], v[168:169]
	s_waitcnt lgkmcnt(1)
	v_mfma_f32_32x32x16_bf16 v[2:17], v[90:93], v[94:97], v[2:17]
	v_fma_f32 v54, v158, v54, v166
	v_fma_f32 v55, v159, v55, v167
	v_fma_f32 v52, v72, v52, v76
	v_fma_f32 v53, v73, v53, v77
	v_fma_f32 v50, v70, v50, v74
	v_fma_f32 v51, v71, v51, v75
	v_pk_fma_f32 v[48:49], v[80:81], v[156:157], v[182:183]
	v_pk_fma_f32 v[46:47], v[78:79], v[114:115], v[180:181]
	v_pk_fma_f32 v[44:45], v[164:165], v[110:111], v[178:179]
	v_pk_fma_f32 v[42:43], v[162:163], v[102:103], v[176:177]
	v_mfma_f32_32x32x16_bf16 v[18:33], v[90:93], v[98:101], v[18:33]
	ds_read_b128 v[90:93], v212 offset:20480
	v_fma_f32 v40, v160, v154, v168
	v_fma_f32 v41, v161, v155, v169
	v_fma_f32 v38, v158, v116, v166
	v_fma_f32 v39, v159, v117, v167
	v_pk_fma_f32 v[36:37], v[72:73], v[112:113], v[76:77]
	v_pk_fma_f32 v[34:35], v[70:71], v[104:105], v[74:75]
	s_waitcnt lgkmcnt(1)
	v_mfma_f32_32x32x16_bf16 v[50:65], v[184:187], v[86:89], v[50:65]
	ds_read_b128 v[70:73], v174 offset:32928
	ds_read_b128 v[74:77], v174 offset:32960
	ds_read_b128 v[78:81], v174 offset:32992
	ds_read_b128 v[86:89], v174 offset:33024
	ds_read_b128 v[110:113], v212 offset:1024
	v_mfma_f32_32x32x16_bf16 v[34:49], v[184:187], v[188:191], v[34:49]
	s_waitcnt lgkmcnt(5)
	v_mfma_f32_32x32x16_bf16 v[50:65], v[90:93], v[94:97], v[50:65]
	v_mfma_f32_32x32x16_bf16 v[34:49], v[90:93], v[98:101], v[34:49]
	s_waitcnt lgkmcnt(2)
	v_mfma_f32_32x32x16_bf16 v[90:105], v[106:109], v[126:129], v[66:81]
	v_mfma_f32_32x32x16_bf16 v[66:81], v[106:109], v[134:137], v[66:81]
	ds_read_b128 v[106:109], v212 offset:0
	s_waitcnt lgkmcnt(0)
	v_mfma_f32_32x32x16_bf16 v[90:105], v[106:109], v[122:125], v[90:105]
	v_mfma_f32_32x32x16_bf16 v[66:81], v[106:109], v[146:149], v[66:81]
	ds_read_b128 v[106:109], v212 offset:2048
	v_mfma_f32_32x32x16_bf16 v[90:105], v[110:113], v[130:133], v[90:105]
	v_mfma_f32_32x32x16_bf16 v[66:81], v[110:113], v[142:145], v[66:81]
	ds_read_b128 v[110:113], v212 offset:13312
	s_waitcnt lgkmcnt(1)
	v_mfma_f32_32x32x16_bf16 v[90:105], v[106:109], v[118:121], v[90:105]
	v_mfma_f32_32x32x16_bf16 v[66:81], v[106:109], v[138:141], v[66:81]
	s_nop 10
	v_cvt_pk_bf16_f32 v90, v90, v91
	v_cvt_pk_bf16_f32 v91, v92, v93
	v_cvt_pk_bf16_f32 v92, v94, v95
	v_cvt_pk_bf16_f32 v94, v98, v99
	v_cvt_pk_bf16_f32 v95, v100, v101
	ds_read_b128 v[98:101], v212 offset:21504
	v_cvt_pk_bf16_f32 v66, v66, v67
	v_cvt_pk_bf16_f32 v67, v68, v69
	v_cvt_pk_bf16_f32 v68, v70, v71
	v_cvt_pk_bf16_f32 v93, v96, v97
	v_cvt_pk_bf16_f32 v69, v72, v73
	ds_read_b128 v[70:73], v212 offset:14336
	v_pk_max_i16 v90, v90, 0
	v_pk_max_i16 v91, v91, 0
	v_pk_max_i16 v92, v92, 0
	v_pk_max_i16 v93, v93, 0
	v_pk_max_i16 v66, v66, 0
	v_pk_max_i16 v67, v67, 0
	v_pk_max_i16 v68, v68, 0
	v_pk_max_i16 v69, v69, 0
	v_cvt_pk_bf16_f32 v96, v102, v103
	s_waitcnt lgkmcnt(2)
	v_mfma_f32_32x32x16_bf16 v[2:17], v[110:113], v[90:93], v[2:17]
	v_cvt_pk_bf16_f32 v97, v104, v105
	v_cvt_pk_bf16_f32 v74, v74, v75
	v_cvt_pk_bf16_f32 v75, v76, v77
	v_cvt_pk_bf16_f32 v76, v78, v79
	v_cvt_pk_bf16_f32 v77, v80, v81
	v_pk_max_i16 v94, v94, 0
	v_pk_max_i16 v95, v95, 0
	v_pk_max_i16 v96, v96, 0
	v_pk_max_i16 v97, v97, 0
	v_pk_max_i16 v74, v74, 0
	v_pk_max_i16 v75, v75, 0
	v_pk_max_i16 v76, v76, 0
	v_pk_max_i16 v77, v77, 0
	v_mfma_f32_32x32x16_bf16 v[18:33], v[110:113], v[66:69], v[18:33]
	s_waitcnt lgkmcnt(1)
	v_mfma_f32_32x32x16_bf16 v[34:49], v[98:101], v[66:69], v[34:49]
	ds_read_b128 v[66:69], v212 offset:22528
	v_mfma_f32_32x32x16_bf16 v[50:65], v[98:101], v[90:93], v[50:65]
	s_waitcnt lgkmcnt(1)
	v_mfma_f32_32x32x16_bf16 v[2:17], v[70:73], v[94:97], v[2:17]
	v_mfma_f32_32x32x16_bf16 v[18:33], v[70:73], v[74:77], v[18:33]
	ds_read_b128 v[78:81], v212 offset:3072
	s_waitcnt lgkmcnt(1)
	v_mfma_f32_32x32x16_bf16 v[50:65], v[66:69], v[94:97], v[50:65]
	ds_read_b128 v[90:93], v174 offset:33056
	ds_read_b128 v[94:97], v174 offset:33088
	ds_read_b128 v[98:101], v174 offset:33120
	ds_read_b128 v[70:73], v174 offset:33152
	v_mfma_f32_32x32x16_bf16 v[34:49], v[66:69], v[74:77], v[34:49]
	ds_read_b128 v[66:69], v212 offset:4096
	ds_read_b128 v[74:77], v212 offset:5120
	s_waitcnt lgkmcnt(3)
	v_mfma_f32_32x32x16_bf16 v[102:117], v[78:81], v[126:129], v[86:101]
	v_mfma_f32_32x32x16_bf16 v[86:101], v[78:81], v[134:137], v[86:101]
	s_waitcnt lgkmcnt(1)
	v_mfma_f32_32x32x16_bf16 v[86:101], v[66:69], v[146:149], v[86:101]
	v_mfma_f32_32x32x16_bf16 v[102:117], v[66:69], v[122:125], v[102:117]
	ds_read_b128 v[66:69], v212 offset:6144
	s_waitcnt lgkmcnt(1)
	v_mfma_f32_32x32x16_bf16 v[86:101], v[74:77], v[142:145], v[86:101]
	v_mfma_f32_32x32x16_bf16 v[102:117], v[74:77], v[130:133], v[102:117]
	ds_read_b128 v[74:77], v212 offset:15360
	s_waitcnt lgkmcnt(1)
	v_mfma_f32_32x32x16_bf16 v[86:101], v[66:69], v[138:141], v[86:101]
	v_mfma_f32_32x32x16_bf16 v[102:117], v[66:69], v[118:121], v[102:117]
	s_nop 10
	v_cvt_pk_bf16_f32 v78, v86, v87
	v_cvt_pk_bf16_f32 v80, v90, v91
	v_cvt_pk_bf16_f32 v79, v88, v89
	v_cvt_pk_bf16_f32 v81, v92, v93
	ds_read_b128 v[86:89], v212 offset:16384
	ds_read_b128 v[90:93], v212 offset:23552
	v_cvt_pk_bf16_f32 v66, v102, v103
	v_cvt_pk_bf16_f32 v67, v104, v105
	v_cvt_pk_bf16_f32 v68, v106, v107
	v_cvt_pk_bf16_f32 v69, v108, v109
	v_pk_max_i16 v66, v66, 0
	v_pk_max_i16 v67, v67, 0
	v_pk_max_i16 v68, v68, 0
	v_pk_max_i16 v69, v69, 0
	v_pk_max_i16 v78, v78, 0
	v_pk_max_i16 v79, v79, 0
	v_pk_max_i16 v80, v80, 0
	v_pk_max_i16 v81, v81, 0
	v_cvt_pk_bf16_f32 v94, v94, v95
	s_waitcnt lgkmcnt(2)
	v_mfma_f32_32x32x16_bf16 v[18:33], v[74:77], v[78:81], v[18:33]
	v_cvt_pk_bf16_f32 v95, v96, v97
	v_cvt_pk_bf16_f32 v96, v98, v99
	v_cvt_pk_bf16_f32 v97, v100, v101
	v_pk_max_i16 v94, v94, 0
	v_pk_max_i16 v95, v95, 0
	v_pk_max_i16 v96, v96, 0
	v_pk_max_i16 v97, v97, 0
	v_mfma_f32_32x32x16_bf16 v[2:17], v[74:77], v[66:69], v[2:17]
	v_cvt_pk_bf16_f32 v74, v110, v111
	v_cvt_pk_bf16_f32 v75, v112, v113
	v_cvt_pk_bf16_f32 v76, v114, v115
	v_cvt_pk_bf16_f32 v77, v116, v117
	v_pk_max_i16 v74, v74, 0
	v_pk_max_i16 v75, v75, 0
	v_pk_max_i16 v76, v76, 0
	v_pk_max_i16 v77, v77, 0
	s_waitcnt lgkmcnt(0)
	v_mfma_f32_32x32x16_bf16 v[50:65], v[90:93], v[66:69], v[50:65]
	ds_read_b128 v[66:69], v212 offset:24576
	v_mfma_f32_32x32x16_bf16 v[34:49], v[90:93], v[78:81], v[34:49]
	ds_read_b128 v[102:105], v212 offset:7168
	v_mfma_f32_32x32x16_bf16 v[2:17], v[86:89], v[74:77], v[2:17]
	s_waitcnt lgkmcnt(1)
	v_mfma_f32_32x32x16_bf16 v[50:65], v[66:69], v[74:77], v[50:65]
	ds_read_b128 v[74:77], v174 offset:33184
	ds_read_b128 v[78:81], v174 offset:33216
	v_mfma_f32_32x32x16_bf16 v[34:49], v[66:69], v[94:97], v[34:49]
	ds_read_b128 v[66:69], v212 offset:8192
	v_mfma_f32_32x32x16_bf16 v[18:33], v[86:89], v[94:97], v[18:33]
	s_waitcnt lgkmcnt(1)
	v_mfma_f32_32x32x16_bf16 v[86:101], v[102:105], v[126:129], v[70:85]
	v_mfma_f32_32x32x16_bf16 v[70:85], v[102:105], v[134:137], v[70:85]
	ds_read_b128 v[102:105], v212 offset:9216
	v_lshlrev_b32_e32 v135, 2, v1
	v_add_u32_e32 v134, v172, v174
	s_waitcnt lgkmcnt(1)
	v_mfma_f32_32x32x16_bf16 v[86:101], v[66:69], v[122:125], v[86:101]
	v_mfma_f32_32x32x16_bf16 v[70:85], v[66:69], v[146:149], v[70:85]
	ds_read_b128 v[66:69], v212 offset:10240
	s_waitcnt lgkmcnt(1)
	v_mfma_f32_32x32x16_bf16 v[86:101], v[102:105], v[130:133], v[86:101]
	v_mfma_f32_32x32x16_bf16 v[70:85], v[102:105], v[142:145], v[70:85]
	ds_read_b128 v[102:105], v212 offset:17408
	s_waitcnt lgkmcnt(1)
	v_mfma_f32_32x32x16_bf16 v[86:101], v[66:69], v[118:121], v[86:101]
	v_mfma_f32_32x32x16_bf16 v[70:85], v[66:69], v[138:141], v[70:85]
	s_nop 10
	v_cvt_pk_bf16_f32 v68, v90, v91
	v_cvt_pk_bf16_f32 v69, v92, v93
	ds_read_b128 v[90:93], v212 offset:25600
	v_cvt_pk_bf16_f32 v66, v86, v87
	v_cvt_pk_bf16_f32 v67, v88, v89
	v_pk_max_i16 v66, v66, 0
	v_pk_max_i16 v67, v67, 0
	v_pk_max_i16 v68, v68, 0
	v_pk_max_i16 v69, v69, 0
	v_cvt_pk_bf16_f32 v70, v70, v71
	v_cvt_pk_bf16_f32 v71, v72, v73
	s_waitcnt lgkmcnt(1)
	v_mfma_f32_32x32x16_bf16 v[2:17], v[102:105], v[66:69], v[2:17]
	v_cvt_pk_bf16_f32 v72, v74, v75
	v_cvt_pk_bf16_f32 v73, v76, v77
	ds_read_b128 v[74:77], v212 offset:18432
	v_cvt_pk_bf16_f32 v86, v94, v95
	v_cvt_pk_bf16_f32 v87, v96, v97
	v_cvt_pk_bf16_f32 v88, v98, v99
	s_waitcnt lgkmcnt(1)
	v_mfma_f32_32x32x16_bf16 v[50:65], v[90:93], v[66:69], v[50:65]
	ds_read_b128 v[66:69], v212 offset:26624
	v_cvt_pk_bf16_f32 v89, v100, v101
	v_pk_max_i16 v86, v86, 0
	v_pk_max_i16 v87, v87, 0
	v_pk_max_i16 v88, v88, 0
	v_pk_max_i16 v89, v89, 0
	v_pk_max_i16 v70, v70, 0
	v_pk_max_i16 v71, v71, 0
	v_pk_max_i16 v72, v72, 0
	v_pk_max_i16 v73, v73, 0
	v_cvt_pk_bf16_f32 v78, v78, v79
	v_cvt_pk_bf16_f32 v79, v80, v81
	s_waitcnt lgkmcnt(1)
	v_mfma_f32_32x32x16_bf16 v[2:17], v[74:77], v[86:89], v[2:17]
	v_cvt_pk_bf16_f32 v80, v82, v83
	v_cvt_pk_bf16_f32 v81, v84, v85
	v_pk_max_i16 v78, v78, 0
	v_pk_max_i16 v79, v79, 0
	v_pk_max_i16 v80, v80, 0
	v_pk_max_i16 v81, v81, 0
	s_waitcnt lgkmcnt(0)
	v_mfma_f32_32x32x16_bf16 v[50:65], v[66:69], v[86:89], v[50:65]
	v_mfma_f32_32x32x16_bf16 v[34:49], v[90:93], v[70:73], v[34:49]
	s_nop 10
	v_add_f32_e32 v130, v10, v58
	v_add_f32_e32 v131, v11, v59
	v_add_f32_e32 v132, v12, v60
	v_add_f32_e32 v133, v13, v61
	v_add_f32_e32 v138, v4, v52
	v_add_f32_e32 v139, v5, v53
	v_pk_add_f32 v[140:141], v[16:17], v[64:65]
	v_pk_add_f32 v[142:143], v[8:9], v[56:57]
	v_pk_add_f32 v[144:145], v[14:15], v[62:63]
	v_pk_add_f32 v[146:147], v[6:7], v[54:55]
	v_mfma_f32_32x32x16_bf16 v[18:33], v[102:105], v[70:73], v[18:33]
	ds_read2st64_b32 v[70:71], v135 offset0:133 offset1:134
	v_add_f32_e32 v148, v2, v50
	v_add_f32_e32 v149, v3, v51
	v_add_f32_e32 v144, v146, v144
	v_add_f32_e32 v145, v147, v145
	v_pk_add_f32 v[140:141], v[142:143], v[140:141]
	v_pk_add_f32 v[132:133], v[138:139], v[132:133]
	v_pk_add_f32 v[130:131], v[148:149], v[130:131]
	v_pk_add_f32 v[132:133], v[132:133], v[140:141]
	v_pk_add_f32 v[130:131], v[130:131], v[144:145]
	v_mfma_f32_32x32x16_bf16 v[34:49], v[66:69], v[78:81], v[34:49]
	s_waitcnt vmcnt(0) lgkmcnt(0)
	v_mul_f32_e32 v66, v175, v70
	v_add_f32_e32 v130, v131, v130
	v_add_f32_e32 v131, v132, v133
	ds_write_b32 v173, v66 offset:512
	v_mul_f32_e32 v66, v175, v71
	v_add_f32_e32 v130, v130, v131
	s_waitcnt lgkmcnt(0)
	ds_read_b128 v[102:105], v174 offset:34560
	ds_read_b128 v[98:101], v174 offset:34592
	ds_read_b128 v[110:113], v174 offset:34624
	ds_read_b128 v[106:109], v174 offset:34656
	ds_read_b128 v[114:117], v174 offset:34688
	ds_read_b128 v[122:125], v174 offset:34720
	ds_read_b128 v[118:121], v174 offset:34752
	ds_read_b128 v[126:129], v174 offset:34784
	v_mov_b32_dpp v66, v66 quad_perm:[1,0,3,2] row_mask:0xf bank_mask:0xf bound_ctrl:1
	v_mov_b32_e32 v131, v130
	v_fmac_f32_e32 v66, v175, v71
	s_nop 0
	v_permlane32_swap_b32_e32 v130, v131
	v_add_f32_dpp v66, v66, v66 quad_perm:[2,3,0,1] row_mask:0xf bank_mask:0xf bound_ctrl:1
	v_add_f32_e32 v130, v130, v131
	v_fmamk_f32 v65, v130, 0xbc800000, v65
	v_add_f32_dpp v66, v66, v66 row_half_mirror row_mask:0xf bank_mask:0xf bound_ctrl:1
	v_fmamk_f32 v64, v130, 0xbc800000, v64
	v_fmamk_f32 v63, v130, 0xbc800000, v63
	v_fmamk_f32 v62, v130, 0xbc800000, v62
	v_fmamk_f32 v61, v130, 0xbc800000, v61
	v_fmamk_f32 v60, v130, 0xbc800000, v60
	v_fmamk_f32 v59, v130, 0xbc800000, v59
	v_fmamk_f32 v58, v130, 0xbc800000, v58
	v_fmamk_f32 v57, v130, 0xbc800000, v57
	v_fmamk_f32 v56, v130, 0xbc800000, v56
	v_fmamk_f32 v55, v130, 0xbc800000, v55
	v_fmamk_f32 v54, v130, 0xbc800000, v54
	v_fmamk_f32 v53, v130, 0xbc800000, v53
	v_fmamk_f32 v52, v130, 0xbc800000, v52
	v_fmamk_f32 v51, v130, 0xbc800000, v51
	v_fmac_f32_e32 v50, 0xbc800000, v130
	v_add_f32_dpp v66, v66, v66 row_ror:8 row_mask:0xf bank_mask:0xf bound_ctrl:1
	v_fmamk_f32 v17, v130, 0xbc800000, v17
	v_fmamk_f32 v16, v130, 0xbc800000, v16
	v_fmamk_f32 v15, v130, 0xbc800000, v15
	v_fmamk_f32 v14, v130, 0xbc800000, v14
	v_fmamk_f32 v13, v130, 0xbc800000, v13
	v_fmamk_f32 v12, v130, 0xbc800000, v12
	v_fmamk_f32 v11, v130, 0xbc800000, v11
	v_fmamk_f32 v10, v130, 0xbc800000, v10
	v_fmamk_f32 v9, v130, 0xbc800000, v9
	v_fmamk_f32 v8, v130, 0xbc800000, v8
	v_fmamk_f32 v7, v130, 0xbc800000, v7
	v_fmamk_f32 v6, v130, 0xbc800000, v6
	v_fmamk_f32 v5, v130, 0xbc800000, v5
	v_fmamk_f32 v4, v130, 0xbc800000, v4
	v_fmamk_f32 v3, v130, 0xbc800000, v3
	v_fmac_f32_e32 v2, 0xbc800000, v130
	v_pk_mul_f32 v[130:131], v[54:55], v[54:55]
	v_pk_mul_f32 v[132:133], v[62:63], v[62:63]
	v_pk_mul_f32 v[138:139], v[50:51], v[50:51]
	v_pk_mul_f32 v[140:141], v[58:59], v[58:59]
	v_pk_mul_f32 v[142:143], v[56:57], v[56:57]
	v_pk_mul_f32 v[144:145], v[64:65], v[64:65]
	v_pk_mul_f32 v[146:147], v[52:53], v[52:53]
	v_pk_mul_f32 v[148:149], v[60:61], v[60:61]
	v_mov_b32_e32 v67, v66
	v_pk_fma_f32 v[148:149], v[12:13], v[12:13], v[148:149]
	v_pk_fma_f32 v[146:147], v[4:5], v[4:5], v[146:147]
	v_pk_fma_f32 v[144:145], v[16:17], v[16:17], v[144:145]
	v_pk_fma_f32 v[142:143], v[8:9], v[8:9], v[142:143]
	v_pk_fma_f32 v[140:141], v[10:11], v[10:11], v[140:141]
	v_pk_fma_f32 v[138:139], v[2:3], v[2:3], v[138:139]
	v_pk_fma_f32 v[132:133], v[14:15], v[14:15], v[132:133]
	v_pk_fma_f32 v[130:131], v[6:7], v[6:7], v[130:131]
	v_permlane16_swap_b32_e32 v66, v67
	v_pk_add_f32 v[130:131], v[130:131], v[132:133]
	v_pk_add_f32 v[132:133], v[138:139], v[140:141]
	v_pk_add_f32 v[138:139], v[142:143], v[144:145]
	v_pk_add_f32 v[140:141], v[146:147], v[148:149]
	v_mfma_f32_32x32x16_bf16 v[18:33], v[74:77], v[78:81], v[18:33]
	v_add_f32_e32 v136, v66, v67
	ds_read_b128 v[70:73], v134 offset:512
	ds_read_b128 v[66:69], v134 offset:544
	ds_read_b128 v[78:81], v134 offset:576
	ds_read_b128 v[74:77], v134 offset:608
	ds_read_b128 v[82:85], v134 offset:640
	ds_read_b128 v[90:93], v134 offset:672
	ds_read_b128 v[86:89], v134 offset:704
	ds_read_b128 v[94:97], v134 offset:736
	v_pk_add_f32 v[138:139], v[140:141], v[138:139]
	v_pk_add_f32 v[130:131], v[132:133], v[130:131]
	s_waitcnt lgkmcnt(8)
	v_pk_mul_f32 v[140:141], v[126:127], v[62:63]
	v_pk_mov_b32 v[132:133], v[130:131], v[138:139] op_sel:[1,0]
	v_mov_b32_e32 v131, v139
	v_pk_mul_f32 v[138:139], v[122:123], v[54:55]
	v_pk_mul_f32 v[142:143], v[114:115], v[50:51]
	v_pk_mul_f32 v[144:145], v[118:119], v[58:59]
	v_pk_mul_f32 v[146:147], v[124:125], v[56:57]
	v_pk_mul_f32 v[148:149], v[128:129], v[64:65]
	v_pk_mul_f32 v[154:155], v[116:117], v[52:53]
	v_pk_mul_f32 v[156:157], v[120:121], v[60:61]
	v_pk_fma_f32 v[154:155], v[104:105], v[4:5], v[154:155]
	v_pk_fma_f32 v[156:157], v[112:113], v[12:13], v[156:157]
	v_pk_fma_f32 v[148:149], v[108:109], v[16:17], v[148:149]
	v_pk_fma_f32 v[146:147], v[100:101], v[8:9], v[146:147]
	v_pk_fma_f32 v[144:145], v[110:111], v[10:11], v[144:145]
	v_pk_fma_f32 v[142:143], v[102:103], v[2:3], v[142:143]
	v_pk_fma_f32 v[140:141], v[106:107], v[14:15], v[140:141]
	v_pk_fma_f32 v[138:139], v[98:99], v[6:7], v[138:139]
	v_pk_add_f32 v[130:131], v[132:133], v[130:131]
	v_pk_add_f32 v[138:139], v[138:139], v[140:141]
	v_pk_add_f32 v[140:141], v[142:143], v[144:145]
	v_pk_add_f32 v[142:143], v[146:147], v[148:149]
	v_pk_add_f32 v[144:145], v[154:155], v[156:157]
	v_pk_add_f32 v[132:133], v[130:131], v[130:131] op_sel:[0,1] op_sel_hi:[1,0]
	v_pk_add_f32 v[142:143], v[144:145], v[142:143]
	v_pk_add_f32 v[138:139], v[140:141], v[138:139]
	v_add_f32_e32 v133, v142, v143
	v_add_f32_e32 v130, v138, v139
	s_waitcnt lgkmcnt(0)
	v_pk_mul_f32 v[138:139], v[90:91], v[54:55]
	v_pk_mul_f32 v[140:141], v[94:95], v[62:63]
	v_pk_mul_f32 v[142:143], v[82:83], v[50:51]
	v_pk_mul_f32 v[144:145], v[86:87], v[58:59]
	v_pk_mul_f32 v[146:147], v[92:93], v[56:57]
	v_pk_mul_f32 v[148:149], v[96:97], v[64:65]
	v_pk_mul_f32 v[154:155], v[84:85], v[52:53]
	v_pk_mul_f32 v[156:157], v[88:89], v[60:61]
	v_add_f32_e32 v130, v130, v133
	v_pk_fma_f32 v[156:157], v[80:81], v[12:13], v[156:157]
	v_pk_fma_f32 v[154:155], v[72:73], v[4:5], v[154:155]
	v_pk_fma_f32 v[148:149], v[76:77], v[16:17], v[148:149]
	v_pk_fma_f32 v[146:147], v[68:69], v[8:9], v[146:147]
	v_pk_fma_f32 v[144:145], v[78:79], v[10:11], v[144:145]
	v_pk_fma_f32 v[142:143], v[70:71], v[2:3], v[142:143]
	v_pk_fma_f32 v[140:141], v[74:75], v[14:15], v[140:141]
	v_pk_fma_f32 v[138:139], v[66:67], v[6:7], v[138:139]
	v_mov_b32_e32 v133, v130
	v_pk_add_f32 v[138:139], v[138:139], v[140:141]
	v_pk_add_f32 v[140:141], v[142:143], v[144:145]
	v_pk_add_f32 v[142:143], v[146:147], v[148:149]
	v_pk_add_f32 v[144:145], v[154:155], v[156:157]
	v_permlane32_swap_b32_e32 v130, v133
	v_pk_add_f32 v[142:143], v[144:145], v[142:143]
	v_add_f32_e32 v160, v130, v133
	v_pk_add_f32 v[138:139], v[140:141], v[138:139]
	v_add_f32_e32 v133, v142, v143
	v_pk_add_f32 v[140:141], v[26:27], v[42:43]
	v_pk_add_f32 v[142:143], v[28:29], v[44:45]
	v_pk_add_f32 v[144:145], v[20:21], v[36:37]
	v_pk_add_f32 v[146:147], v[32:33], v[48:49]
	v_pk_add_f32 v[148:149], v[24:25], v[40:41]
	v_pk_add_f32 v[154:155], v[30:31], v[46:47]
	v_pk_add_f32 v[156:157], v[22:23], v[38:39]
	v_pk_add_f32 v[158:159], v[18:19], v[34:35]
	v_pk_add_f32 v[154:155], v[156:157], v[154:155]
	v_pk_add_f32 v[146:147], v[148:149], v[146:147]
	v_pk_add_f32 v[142:143], v[144:145], v[142:143]
	v_pk_add_f32 v[140:141], v[158:159], v[140:141]
	v_pk_add_f32 v[142:143], v[142:143], v[146:147]
	v_pk_add_f32 v[140:141], v[140:141], v[154:155]
	v_add_f32_e32 v130, v138, v139
	v_add_f32_e32 v140, v141, v140
	v_add_f32_e32 v141, v142, v143
	v_add_f32_e32 v133, v130, v133
	v_add_f32_e32 v140, v140, v141
	v_mov_b32_e32 v131, v132
	v_mov_b32_e32 v130, v140
	s_nop 1
	v_permlane32_swap_b32_e32 v140, v130
	v_add_f32_e32 v130, v140, v130
	v_fmamk_f32 v49, v130, 0xbc800000, v49
	v_fmamk_f32 v48, v130, 0xbc800000, v48
	v_fmamk_f32 v47, v130, 0xbc800000, v47
	v_fmamk_f32 v46, v130, 0xbc800000, v46
	v_fmamk_f32 v45, v130, 0xbc800000, v45
	v_fmamk_f32 v44, v130, 0xbc800000, v44
	v_fmamk_f32 v43, v130, 0xbc800000, v43
	v_fmamk_f32 v42, v130, 0xbc800000, v42
	v_fmamk_f32 v41, v130, 0xbc800000, v41
	v_fmamk_f32 v40, v130, 0xbc800000, v40
	v_fmamk_f32 v39, v130, 0xbc800000, v39
	v_fmamk_f32 v38, v130, 0xbc800000, v38
	v_fmamk_f32 v37, v130, 0xbc800000, v37
	v_fmamk_f32 v36, v130, 0xbc800000, v36
	v_fmamk_f32 v35, v130, 0xbc800000, v35
	v_fmac_f32_e32 v34, 0xbc800000, v130
	v_fmamk_f32 v33, v130, 0xbc800000, v33
	v_fmamk_f32 v32, v130, 0xbc800000, v32
	v_fmamk_f32 v31, v130, 0xbc800000, v31
	v_fmamk_f32 v30, v130, 0xbc800000, v30
	v_fmamk_f32 v29, v130, 0xbc800000, v29
	v_fmamk_f32 v28, v130, 0xbc800000, v28
	v_fmamk_f32 v27, v130, 0xbc800000, v27
	v_fmamk_f32 v26, v130, 0xbc800000, v26
	v_fmamk_f32 v25, v130, 0xbc800000, v25
	v_fmamk_f32 v24, v130, 0xbc800000, v24
	v_fmamk_f32 v23, v130, 0xbc800000, v23
	v_fmamk_f32 v22, v130, 0xbc800000, v22
	v_fmamk_f32 v21, v130, 0xbc800000, v21
	v_fmamk_f32 v20, v130, 0xbc800000, v20
	v_fmamk_f32 v19, v130, 0xbc800000, v19
	v_fmac_f32_e32 v18, 0xbc800000, v130
	v_pk_mul_f32 v[140:141], v[38:39], v[38:39]
	v_pk_mul_f32 v[142:143], v[46:47], v[46:47]
	v_pk_mul_f32 v[144:145], v[34:35], v[34:35]
	v_pk_mul_f32 v[146:147], v[42:43], v[42:43]
	v_pk_mul_f32 v[148:149], v[40:41], v[40:41]
	v_pk_mul_f32 v[154:155], v[48:49], v[48:49]
	v_pk_mul_f32 v[156:157], v[36:37], v[36:37]
	v_pk_mul_f32 v[158:159], v[44:45], v[44:45]
	v_pk_fma_f32 v[156:157], v[20:21], v[20:21], v[156:157]
	v_pk_fma_f32 v[158:159], v[28:29], v[28:29], v[158:159]
	v_pk_fma_f32 v[154:155], v[32:33], v[32:33], v[154:155]
	v_pk_fma_f32 v[148:149], v[24:25], v[24:25], v[148:149]
	v_pk_fma_f32 v[146:147], v[26:27], v[26:27], v[146:147]
	v_pk_fma_f32 v[144:145], v[18:19], v[18:19], v[144:145]
	v_pk_fma_f32 v[142:143], v[30:31], v[30:31], v[142:143]
	v_pk_fma_f32 v[140:141], v[22:23], v[22:23], v[140:141]
	v_permlane32_swap_b32_e32 v132, v131
	v_pk_add_f32 v[140:141], v[140:141], v[142:143]
	v_pk_add_f32 v[142:143], v[144:145], v[146:147]
	v_pk_add_f32 v[144:145], v[148:149], v[154:155]
	v_pk_add_f32 v[146:147], v[156:157], v[158:159]
	v_pk_add_f32 v[140:141], v[142:143], v[140:141]
	v_pk_add_f32 v[144:145], v[146:147], v[144:145]
	v_pk_mul_f32 v[122:123], v[122:123], v[38:39]
	v_pk_mov_b32 v[142:143], v[140:141], v[144:145] op_sel:[1,0]
	v_mov_b32_e32 v141, v145
	v_pk_add_f32 v[140:141], v[142:143], v[140:141]
	v_pk_mul_f32 v[126:127], v[126:127], v[46:47]
	v_pk_add_f32 v[140:141], v[140:141], v[140:141] op_sel:[0,1] op_sel_hi:[1,0]
	v_pk_mul_f32 v[114:115], v[114:115], v[34:35]
	v_mov_b32_e32 v130, v140
	s_nop 1
	v_permlane32_swap_b32_e32 v140, v130
	v_mov_b32_e32 v141, v132
	v_pk_add_f32 v[130:131], v[140:141], v[130:131]
	v_pk_mul_f32 v[118:119], v[118:119], v[42:43]
	v_pk_fma_f32 v[130:131], v[130:131], s[0:1], v[152:153] op_sel_hi:[1,0,0]
	v_pk_mul_f32 v[124:125], v[124:125], v[40:41]
	v_pk_mul_f32 v[128:129], v[128:129], v[48:49]
	v_pk_mul_f32 v[116:117], v[116:117], v[36:37]
	v_pk_mul_f32 v[120:121], v[120:121], v[44:45]
	v_pk_fma_f32 v[112:113], v[112:113], v[28:29], v[120:121]
	v_pk_fma_f32 v[104:105], v[104:105], v[20:21], v[116:117]
	v_pk_fma_f32 v[108:109], v[108:109], v[32:33], v[128:129]
	v_pk_fma_f32 v[100:101], v[100:101], v[24:25], v[124:125]
	v_pk_fma_f32 v[110:111], v[110:111], v[26:27], v[118:119]
	v_pk_fma_f32 v[102:103], v[102:103], v[18:19], v[114:115]
	v_pk_fma_f32 v[106:107], v[106:107], v[30:31], v[126:127]
	v_pk_fma_f32 v[98:99], v[98:99], v[22:23], v[122:123]
	v_rsq_f32_e32 v131, v131
	v_pk_add_f32 v[98:99], v[98:99], v[106:107]
	v_pk_add_f32 v[102:103], v[102:103], v[110:111]
	v_pk_add_f32 v[100:101], v[100:101], v[108:109]
	v_pk_add_f32 v[104:105], v[104:105], v[112:113]
	v_rsq_f32_e32 v132, v130
	v_pk_add_f32 v[100:101], v[104:105], v[100:101]
	v_pk_add_f32 v[98:99], v[102:103], v[98:99]
	v_add_f32_e32 v98, v98, v99
	v_add_f32_e32 v99, v100, v101
	v_add_f32_e32 v98, v98, v99
	v_mov_b32_e32 v99, v98
	v_pk_mul_f32 v[90:91], v[90:91], v[38:39]
	v_pk_mul_f32 v[94:95], v[94:95], v[46:47]
	v_pk_mul_f32 v[82:83], v[82:83], v[34:35]
	v_pk_mul_f32 v[86:87], v[86:87], v[42:43]
	v_permlane32_swap_b32_e32 v98, v99
	v_pk_fma_f32 v[78:79], v[78:79], v[26:27], v[86:87]
	v_pk_fma_f32 v[70:71], v[70:71], v[18:19], v[82:83]
	v_pk_fma_f32 v[74:75], v[74:75], v[30:31], v[94:95]
	v_pk_fma_f32 v[66:67], v[66:67], v[22:23], v[90:91]
	v_mov_b32_e32 v130, v131
	v_mov_b32_e32 v131, v132
	v_add_f32_e32 v98, v98, v99
	v_pk_add_f32 v[66:67], v[66:67], v[74:75]
	v_pk_add_f32 v[70:71], v[70:71], v[78:79]
	v_mul_f32_e32 v139, v160, v130
	v_mul_f32_e32 v98, v98, v131
	v_pk_add_f32 v[66:67], v[70:71], v[66:67]
	v_cmp_gt_u32_e32 vcc, 32, v1
	v_add_f32_e32 v66, v66, v67
	v_pk_mul_f32 v[92:93], v[92:93], v[40:41]
	v_cndmask_b32_e32 v67, v98, v139, vcc
	v_add_f32_e32 v67, s12, v67
	v_pk_mul_f32 v[96:97], v[96:97], v[48:49]
	v_pk_mul_f32 v[84:85], v[84:85], v[36:37]
	v_pk_mul_f32 v[88:89], v[88:89], v[44:45]
	v_mul_f32_e32 v67, 0xbfb8aa3b, v67
	v_pk_fma_f32 v[80:81], v[80:81], v[28:29], v[88:89]
	v_pk_fma_f32 v[72:73], v[72:73], v[20:21], v[84:85]
	v_pk_fma_f32 v[76:77], v[76:77], v[32:33], v[96:97]
	v_pk_fma_f32 v[68:69], v[68:69], v[24:25], v[92:93]
	v_exp_f32_e32 v70, v67
	v_pk_add_f32 v[68:69], v[68:69], v[76:77]
	v_pk_add_f32 v[72:73], v[72:73], v[80:81]
	v_cmp_lt_i32_e64 s[0:1], 0, v151
	v_pk_add_f32 v[68:69], v[72:73], v[68:69]
	v_mov_b32_e32 v137, v136
	v_add_f32_e32 v67, v68, v69
	v_add_f32_e32 v67, v66, v67
	v_add_f32_e32 v66, 1.0, v70
	v_rcp_f32_e32 v66, v66
	v_mov_b32_e32 v69, 0xff800000
	v_mov_b32_e32 v138, v133
	v_mov_b32_e32 v68, v67
	v_cndmask_b32_e64 v70, v69, v66, s[0:1]
	v_mbcnt_lo_u32_b32 v66, -1, 0
	v_mbcnt_hi_u32_b32 v66, -1, v66
	v_permlane32_swap_b32_e32 v136, v137
	v_permlane32_swap_b32_e32 v133, v138
	v_permlane32_swap_b32_e32 v67, v68
	v_and_b32_e32 v86, 64, v66
	s_mov_b32 s14, 8
	s_mov_b32 s13, 0
	v_mov_b32_e32 v66, 0
	s_waitcnt lgkmcnt(0)

.Ltopk_done:
	v_add_f32_e32 v69, v133, v138
	v_add_f32_e32 v67, v67, v68
	v_mul_f32_e32 v69, v69, v130
	v_mul_f32_e32 v67, v67, v131
	v_add_f32_e32 v68, v136, v137
	v_cndmask_b32_e32 v67, v67, v69, vcc
	v_add_f32_e32 v67, v68, v67
	v_mul_f32_e32 v68, 0x3e000000, v67
	v_mov_b32_e32 v69, 0xff800000
	v_cmp_lt_i32_e64 s[0:1], 0, v66
	s_mov_b32 s4, 0x3e000000
	v_cvt_f32_u32_e32 v66, v66
	v_cndmask_b32_e64 v68, v69, v68, s[0:1]
	v_cvt_pk_bf16_f32 v9, v8, v9
	v_cvt_pk_bf16_f32 v8, v6, v7
	v_max_f32_dpp v68, v68, v68 quad_perm:[1,0,3,2] row_mask:0xf bank_mask:0xf bound_ctrl:1
	v_cvt_pk_bf16_f32 v6, v2, v3
	s_nop 0
	v_max_f32_dpp v68, v68, v68 quad_perm:[2,3,0,1] row_mask:0xf bank_mask:0xf bound_ctrl:1
	v_cvt_pk_bf16_f32 v7, v4, v5
	s_nop 0
	v_max_f32_dpp v68, v68, v68 row_half_mirror row_mask:0xf bank_mask:0xf bound_ctrl:1
	v_cvt_pk_bf16_f32 v91, v16, v17
	v_cvt_pk_bf16_f32 v90, v14, v15
	v_max_f32_dpp v68, v68, v68 row_ror:8 row_mask:0xf bank_mask:0xf bound_ctrl:1
	v_mov_b32_e32 v69, v68
	s_nop 1
	v_permlane16_swap_b32_e32 v68, v69
	v_max_f32_e32 v68, v68, v69
	v_mov_b32_e32 v69, v68
	s_nop 1
	v_permlane32_swap_b32_e32 v68, v69
	v_max_f32_e32 v68, v68, v69
	v_fma_f32 v67, v67, s4, -v68
	v_mul_f32_e32 v67, 0x3fb8aa3b, v67
	v_exp_f32_e32 v67, v67
	v_cvt_pk_bf16_f32 v89, v12, v13
	v_cvt_pk_bf16_f32 v88, v10, v11
	v_mul_f32_e32 v66, v67, v66
	v_cndmask_b32_e64 v66, 0, v66, s[0:1]
	v_cvt_pk_bf16_f32 v57, v56, v57
	v_cvt_pk_bf16_f32 v56, v54, v55
	v_add_f32_dpp v67, v66, v66 quad_perm:[1,0,3,2] row_mask:0xf bank_mask:0xf bound_ctrl:1
	v_cvt_pk_bf16_f32 v54, v50, v51
	v_cvt_pk_bf16_f32 v50, v58, v59
	v_add_f32_dpp v67, v67, v67 quad_perm:[2,3,0,1] row_mask:0xf bank_mask:0xf bound_ctrl:1
	v_cvt_pk_bf16_f32 v55, v52, v53
	s_nop 0
	v_add_f32_dpp v67, v67, v67 row_half_mirror row_mask:0xf bank_mask:0xf bound_ctrl:1
	v_cvt_pk_bf16_f32 v53, v64, v65
	v_cvt_pk_bf16_f32 v52, v62, v63
	v_add_f32_dpp v67, v67, v67 row_ror:8 row_mask:0xf bank_mask:0xf bound_ctrl:1
	v_mov_b32_e32 v68, v67
	s_nop 1
	v_permlane16_swap_b32_e32 v67, v68
	v_add_f32_e32 v67, v67, v68
	v_mov_b32_e32 v68, v67
	s_nop 1
	v_permlane32_swap_b32_e32 v67, v68
	v_add_f32_e32 v67, v67, v68
	v_rcp_f32_e32 v67, v67
	v_cvt_pk_bf16_f32 v51, v60, v61
	v_cvt_pk_bf16_f32 v25, v24, v25
	v_cvt_pk_bf16_f32 v24, v22, v23
	v_mul_f32_e32 v66, v66, v67
	v_cndmask_b32_e32 v67, v131, v130, vcc
	v_mul_f32_e32 v66, v67, v66
	ds_write_b32 v173, v66 offset:768
	s_waitcnt lgkmcnt(0)
	ds_read_b128 v[82:85], v212 offset:27648
	ds_read_b128 v[92:95], v212 offset:28672
	ds_read_b128 v[96:99], v212 offset:31744
	ds_read_b128 v[100:103], v212 offset:32768
	s_waitcnt lgkmcnt(3)
	v_mfma_f32_32x32x16_bf16 v[66:81], v[6:9], v[82:85], 0
	ds_read_b128 v[104:107], v212 offset:29696
	ds_read_b32 v87, v135 offset:34816
	v_cvt_pk_bf16_f32 v23, v20, v21
	v_cvt_pk_bf16_f32 v22, v18, v19
	v_cvt_pk_bf16_f32 v119, v32, v33
	v_cvt_pk_bf16_f32 v118, v30, v31
	v_cvt_pk_bf16_f32 v117, v28, v29
	s_waitcnt lgkmcnt(3)
	v_mfma_f32_32x32x16_bf16 v[2:17], v[6:9], v[96:99], 0
	v_cvt_pk_bf16_f32 v116, v26, v27
	v_cvt_pk_bf16_f32 v41, v40, v41
	v_cvt_pk_bf16_f32 v40, v38, v39
	v_cvt_pk_bf16_f32 v39, v36, v37
	v_cvt_pk_bf16_f32 v38, v34, v35
	v_cvt_pk_bf16_f32 v37, v48, v49
	v_cvt_pk_bf16_f32 v36, v46, v47
	v_mfma_f32_32x32x16_bf16 v[66:81], v[88:91], v[92:95], v[66:81]
	v_cvt_pk_bf16_f32 v35, v44, v45
	v_cvt_pk_bf16_f32 v34, v42, v43
	s_waitcnt lgkmcnt(2)
	v_mfma_f32_32x32x16_bf16 v[2:17], v[88:91], v[100:103], v[2:17]
	ds_read_b128 v[88:91], v212 offset:30720
	ds_read_b128 v[108:111], v212 offset:33792
	s_waitcnt lgkmcnt(3)
	v_mfma_f32_32x32x16_bf16 v[66:81], v[54:57], v[104:107], v[66:81]
	s_waitcnt lgkmcnt(0)
	v_mfma_f32_32x32x16_bf16 v[2:17], v[54:57], v[108:111], v[2:17]
	ds_read_b128 v[112:115], v212 offset:34816
	v_mfma_f32_32x32x16_bf16 v[66:81], v[50:53], v[88:91], v[66:81]
	s_waitcnt lgkmcnt(0)
	v_mfma_f32_32x32x16_bf16 v[2:17], v[50:53], v[112:115], v[2:17]
	v_mfma_f32_32x32x16_bf16 v[50:65], v[22:25], v[82:85], 0
	v_mfma_f32_32x32x16_bf16 v[18:33], v[22:25], v[96:99], 0
	v_mfma_f32_32x32x16_bf16 v[50:65], v[116:119], v[92:95], v[50:65]
	v_mfma_f32_32x32x16_bf16 v[18:33], v[116:119], v[100:103], v[18:33]
	v_mfma_f32_32x32x16_bf16 v[50:65], v[38:41], v[104:107], v[50:65]
	v_mfma_f32_32x32x16_bf16 v[18:33], v[38:41], v[108:111], v[18:33]
	ds_read_b128 v[38:41], v134 offset:896
	ds_read_b128 v[42:45], v134 offset:928
	v_mfma_f32_32x32x16_bf16 v[50:65], v[34:37], v[88:91], v[50:65]
	v_mfma_f32_32x32x16_bf16 v[18:33], v[34:37], v[112:115], v[18:33]
	ds_read_b128 v[34:37], v134 offset:960
	ds_read_b128 v[46:49], v134 offset:992
	ds_read_b128 v[82:85], v134 offset:768
	ds_read_b128 v[88:91], v134 offset:800
	ds_read_b128 v[92:95], v134 offset:832
	ds_read_b128 v[96:99], v134 offset:864
	s_waitcnt lgkmcnt(4)
	s_nop 3
	v_pk_mul_f32 v[54:55], v[42:43], v[54:55]
	v_pk_mul_f32 v[62:63], v[46:47], v[62:63]
	v_pk_mul_f32 v[56:57], v[44:45], v[56:57]
	v_pk_mul_f32 v[64:65], v[48:49], v[64:65]
	v_pk_mul_f32 v[52:53], v[40:41], v[52:53]
	v_pk_mul_f32 v[60:61], v[36:37], v[60:61]
	v_pk_mul_f32 v[58:59], v[34:35], v[58:59]
	v_pk_mul_f32 v[50:51], v[38:39], v[50:51]
	v_pk_mul_f32 v[22:23], v[42:43], v[22:23]
	v_pk_mul_f32 v[30:31], v[46:47], v[30:31]
	v_pk_mul_f32 v[24:25], v[44:45], v[24:25]
	v_pk_mul_f32 v[32:33], v[48:49], v[32:33]
	v_pk_mul_f32 v[20:21], v[40:41], v[20:21]
	v_pk_mul_f32 v[28:29], v[36:37], v[28:29]
	v_pk_mul_f32 v[26:27], v[34:35], v[26:27]
	v_pk_mul_f32 v[18:19], v[38:39], v[18:19]
	s_waitcnt lgkmcnt(0)
	v_pk_fma_f32 v[58:59], v[92:93], v[74:75], v[58:59]
	v_pk_fma_f32 v[60:61], v[94:95], v[76:77], v[60:61]
	v_pk_fma_f32 v[52:53], v[84:85], v[68:69], v[52:53]
	v_pk_fma_f32 v[64:65], v[98:99], v[80:81], v[64:65]
	v_pk_fma_f32 v[56:57], v[90:91], v[72:73], v[56:57]
	v_pk_fma_f32 v[62:63], v[96:97], v[78:79], v[62:63]
	v_pk_fma_f32 v[54:55], v[88:89], v[70:71], v[54:55]
	v_pk_fma_f32 v[50:51], v[82:83], v[66:67], v[50:51]
	v_pk_fma_f32 v[10:11], v[92:93], v[10:11], v[26:27]
	v_pk_fma_f32 v[12:13], v[94:95], v[12:13], v[28:29]
	v_pk_fma_f32 v[4:5], v[84:85], v[4:5], v[20:21]
	v_pk_fma_f32 v[16:17], v[98:99], v[16:17], v[32:33]
	v_pk_fma_f32 v[8:9], v[90:91], v[8:9], v[24:25]
	v_pk_fma_f32 v[14:15], v[96:97], v[14:15], v[30:31]
	v_pk_fma_f32 v[6:7], v[88:89], v[6:7], v[22:23]
	v_pk_fma_f32 v[2:3], v[82:83], v[2:3], v[18:19]
	v_pk_add_f32 v[54:55], v[54:55], v[62:63]
	v_pk_add_f32 v[56:57], v[56:57], v[64:65]
	v_pk_add_f32 v[52:53], v[52:53], v[60:61]
	v_pk_add_f32 v[50:51], v[50:51], v[58:59]
	v_pk_add_f32 v[6:7], v[6:7], v[14:15]
	v_pk_add_f32 v[8:9], v[8:9], v[16:17]
	v_pk_add_f32 v[4:5], v[4:5], v[12:13]
	v_pk_add_f32 v[2:3], v[2:3], v[10:11]
	v_pk_add_f32 v[52:53], v[52:53], v[56:57]
	v_pk_add_f32 v[50:51], v[50:51], v[54:55]
	v_pk_add_f32 v[4:5], v[4:5], v[8:9]
	v_pk_add_f32 v[2:3], v[2:3], v[6:7]
	v_add_f32_e32 v50, v50, v51
	v_add_f32_e32 v51, v52, v53
	v_add_f32_e32 v2, v2, v3
	v_add_f32_e32 v3, v4, v5
	v_add_f32_e32 v50, v50, v51
	v_add_f32_e32 v2, v2, v3
	v_mov_b32_e32 v3, v50
	v_mov_b32_e32 v4, v2
	s_nop 0
	v_permlane32_swap_b32_e32 v50, v3
	v_permlane32_swap_b32_e32 v2, v4
	v_add_f32_e32 v3, v50, v3
	v_add_f32_e32 v2, v2, v4
	v_cndmask_b32_e32 v2, v2, v3, vcc
	v_add_f32_e32 v3, v87, v2
	v_cmp_eq_u32_e32 vcc, 0, v1
	s_nop 0
	v_max_f32_dpp v2, v3, v3 quad_perm:[1,0,3,2] row_mask:0xf bank_mask:0xf bound_ctrl:1
	s_nop 1
	v_max_f32_dpp v2, v2, v2 quad_perm:[2,3,0,1] row_mask:0xf bank_mask:0xf bound_ctrl:1
	s_nop 1
	v_max_f32_dpp v2, v2, v2 row_half_mirror row_mask:0xf bank_mask:0xf bound_ctrl:1
	s_nop 1
	v_max_f32_dpp v2, v2, v2 row_ror:8 row_mask:0xf bank_mask:0xf bound_ctrl:1
	v_mov_b32_e32 v4, v2
	s_nop 1
	v_permlane16_swap_b32_e32 v2, v4
	v_max_f32_e32 v2, v2, v4
	v_mov_b32_e32 v4, v2
	s_nop 1
	v_permlane32_swap_b32_e32 v2, v4
	v_max_f32_e32 v2, v2, v4
	v_sub_f32_e32 v4, v3, v2
	v_mul_f32_e32 v4, 0x3fb8aa3b, v4
	v_exp_f32_e32 v4, v4
	s_nop 1
	v_add_f32_dpp v4, v4, v4 quad_perm:[1,0,3,2] row_mask:0xf bank_mask:0xf bound_ctrl:1
	s_nop 1
	v_add_f32_dpp v4, v4, v4 quad_perm:[2,3,0,1] row_mask:0xf bank_mask:0xf bound_ctrl:1
	s_nop 1
	v_add_f32_dpp v4, v4, v4 row_half_mirror row_mask:0xf bank_mask:0xf bound_ctrl:1
	s_nop 1
	v_add_f32_dpp v4, v4, v4 row_ror:8 row_mask:0xf bank_mask:0xf bound_ctrl:1
	v_mov_b32_e32 v5, v4
	s_nop 1
	v_permlane16_swap_b32_e32 v4, v5
	v_add_f32_e32 v4, v4, v5
	v_and_or_b32 v5, s3, 63, v86
	v_lshlrev_b32_e32 v5, 2, v5
	ds_bpermute_b32 v3, v5, v3
	v_mov_b32_e32 v5, v4
	s_nop 1
	v_permlane32_swap_b32_e32 v4, v5
	s_and_saveexec_b64 s[4:5], vcc
	s_cbranch_execz .LBB1_12
	v_add_f32_e32 v1, v4, v5
	s_mov_b32 s0, 0x800000
	v_cmp_gt_f32_e32 vcc, s0, v1
	s_mov_b32 s0, 0x3f317217
	s_nop 0
	v_cndmask_b32_e64 v4, 0, 32, vcc
	v_ldexp_f32 v1, v1, v4
	v_log_f32_e32 v1, v1
	s_nop 0
	v_mul_f32_e32 v4, 0x3f317217, v1
	v_fma_f32 v4, v1, s0, -v4
	v_fmamk_f32 v4, v1, 0x3377d1cf, v4
	s_mov_b32 s0, 0x7f800000
	v_fmac_f32_e32 v4, 0x3f317217, v1
	v_cmp_lt_f32_e64 s[0:1], |v1|, s0
	s_nop 1
	v_cndmask_b32_e64 v1, v1, v4, s[0:1]
	v_mov_b32_e32 v4, 0x41b17218
	v_cndmask_b32_e32 v4, 0, v4, vcc
	v_sub_f32_e32 v1, v1, v4
	v_add_f32_e32 v1, v2, v1
	s_waitcnt lgkmcnt(0)
	v_sub_f32_e32 v1, v1, v3
	ds_write_b32 v172, v1
